# diff-attention tile loop software-pipelined across tiles (softmax of one map beside PV of the other map and QK of the next tile; one barrier per tile kept)
# speedup vs baseline: 1.0046x; 1.0046x over previous
.LBB0_564:
	s_xor_b64 s[12:13], s[14:15], -1
	s_and_b64 s[14:15], s[14:15], exec
	s_cselect_b32 s39, s31, s34
	s_mul_i32 s14, s39, 0x1a00
	v_mov_b32_e32 v128, v231
	s_add_u32 s16, s6, s14
	s_addc_u32 s17, s7, 0
	v_readfirstlane_b32 s18, v128
	v_lshlrev_b32_e32 v0, 3, v128
	s_ashr_i32 s14, s18, 6
	v_and_b32_e32 v129, 0x78, v0
	v_bfe_u32 v130, v128, 4, 2
	s_lshl_b32 s38, s14, 5
	v_lshlrev_b32_e32 v208, 1, v129
	v_or_b32_e32 v2, 4, v130
	v_or_b32_e32 v8, 8, v130
	v_or_b32_e32 v10, 12, v130
	v_lshl_add_u64 v[28:29], s[16:17], 0, v[208:209]
	v_or_b32_e32 v32, s38, v130
	v_or_b32_e32 v33, s38, v2
	v_or_b32_e32 v34, s38, v8
	v_or_b32_e32 v35, s38, v10
	v_mad_i64_i32 v[0:1], s[16:17], v32, s62, v[28:29]
	v_mad_i64_i32 v[4:5], s[16:17], v33, s62, v[28:29]
	v_mad_i64_i32 v[8:9], s[16:17], v34, s62, v[28:29]
	v_mad_i64_i32 v[12:13], s[16:17], v35, s62, v[28:29]
	global_load_dwordx4 v[0:3], v[0:1], off
	s_nop 0
	global_load_dwordx4 v[4:7], v[4:5], off
	s_nop 0
	global_load_dwordx4 v[8:11], v[8:9], off
	s_nop 0
	global_load_dwordx4 v[12:15], v[12:13], off
	v_or_b32_e32 v36, 16, v32
	v_mad_i64_i32 v[16:17], s[16:17], v36, s62, v[28:29]
	global_load_dwordx4 v[16:19], v[16:17], off
	v_or_b32_e32 v20, 20, v130
	v_or_b32_e32 v37, s38, v20
	v_mad_i64_i32 v[20:21], s[16:17], v37, s62, v[28:29]
	global_load_dwordx4 v[20:23], v[20:21], off
	v_or_b32_e32 v24, 24, v130
	v_or_b32_e32 v38, s38, v24
	v_mad_i64_i32 v[24:25], s[16:17], v38, s62, v[28:29]
	v_or_b32_e32 v30, 28, v130
	global_load_dwordx4 v[24:27], v[24:25], off
	v_or_b32_e32 v39, s38, v30
	v_mad_i64_i32 v[28:29], s[16:17], v39, s62, v[28:29]
	global_load_dwordx4 v[28:31], v[28:29], off
	v_xor_b32_e32 v40, v130, v128
	v_bitop3_b32 v41, v130, v128, 4 bitop3:0x36
	v_bitop3_b32 v42, v130, v128, 8 bitop3:0x36
	v_bitop3_b32 v43, v130, v128, 12 bitop3:0x36
	v_lshlrev_b32_e32 v40, 4, v40
	v_lshlrev_b32_e32 v41, 4, v41
	v_lshlrev_b32_e32 v42, 4, v42
	v_lshlrev_b32_e32 v43, 4, v43
	v_and_b32_e32 v40, 0xf0, v40
	v_lshlrev_b32_e32 v32, 8, v32
	v_and_b32_e32 v41, 0xf0, v41
	v_and_b32_e32 v42, 0xf0, v42
	v_and_b32_e32 v43, 0xf0, v43
	v_lshlrev_b32_e32 v33, 8, v33
	v_lshlrev_b32_e32 v34, 8, v34
	v_lshlrev_b32_e32 v35, 8, v35
	v_add3_u32 v32, s65, v32, v40
	s_and_b32 s16, s18, 0x3fffffc0
	v_add3_u32 v33, s65, v33, v41
	v_add3_u32 v34, s65, v34, v42
	v_add3_u32 v35, s65, v35, v43
	v_lshlrev_b32_e32 v36, 8, v36
	s_lshl_b32 s16, s16, 2
	s_add_i32 s40, s16, 0
	s_lshl_b32 s16, s14, 3
	v_bitop3_b32 v56, s16, v128, v130 bitop3:0x36
	v_or_b32_e32 v55, s16, v130
	v_lshlrev_b32_e32 v56, 3, v56
	v_mul_lo_u32 v57, v55, s96
	v_and_b32_e32 v133, 0x78, v56
	v_bitop3_b32 v55, v55, v128, 4 bitop3:0x36
	v_lshlrev_b32_e32 v132, 5, v130
	v_or_b32_e32 v56, v133, v57
	v_lshlrev_b32_e32 v55, 3, v55
	v_lshlrev_b32_e32 v208, 1, v56
	v_bitop3_b32 v56, v57, v132, v129 bitop3:0xf6
	v_add_u32_e32 v57, 0x3400, v57
	s_waitcnt vmcnt(7)
	ds_write_b128 v32, v[0:3]
	s_waitcnt vmcnt(6)
	ds_write_b128 v33, v[4:7]
	s_waitcnt vmcnt(5)
	ds_write_b128 v34, v[8:11]
	s_waitcnt vmcnt(4)
	ds_write_b128 v35, v[12:15]
	v_bitop3_b32 v1, v130, v128, 20 bitop3:0x36
	v_add3_u32 v0, s65, v36, v40
	v_lshlrev_b32_e32 v1, 4, v1
	s_waitcnt vmcnt(3)
	ds_write_b128 v0, v[16:19]
	v_lshlrev_b32_e32 v0, 8, v37
	v_and_b32_e32 v1, 0xf0, v1
	v_add3_u32 v0, s65, v0, v1
	v_bitop3_b32 v1, v130, v128, 24 bitop3:0x36
	v_lshlrev_b32_e32 v1, 4, v1
	s_waitcnt vmcnt(2)
	ds_write_b128 v0, v[20:23]
	v_lshlrev_b32_e32 v0, 8, v38
	v_and_b32_e32 v1, 0xf0, v1
	v_add3_u32 v0, s65, v0, v1
	v_bitop3_b32 v1, v130, v128, 28 bitop3:0x36
	v_lshlrev_b32_e32 v1, 4, v1
	v_and_b32_e32 v134, 0x78, v55
	s_waitcnt vmcnt(1)
	ds_write_b128 v0, v[24:27]
	v_lshlrev_b32_e32 v0, 8, v39
	v_and_b32_e32 v1, 0xf0, v1
	v_or_b32_e32 v55, v134, v57
	s_lshl_b32 s16, s14, 11
	v_add3_u32 v0, s65, v0, v1
	v_lshlrev_b32_e32 v56, 1, v56
	v_lshlrev_b32_e32 v58, 1, v55
	v_bitop3_b32 v55, v57, v132, v129 bitop3:0xf6
	v_lshl_add_u64 v[62:63], s[6:7], 0, v[208:209]
	s_add_i32 s44, s16, 0
	v_mov_b32_e32 v57, v209
	s_waitcnt vmcnt(0)
	ds_write_b128 v0, v[28:31]
	v_mov_b32_e32 v64, v209
	v_mov_b32_e32 v32, v209
	v_mov_b32_e32 v16, v209
	v_mov_b32_e32 v0, v209
	v_mov_b32_e32 v112, v209
	v_mov_b32_e32 v96, v209
	v_mov_b32_e32 v80, v209
	v_mov_b32_e32 v48, v209
	v_lshl_add_u64 v[62:63], v[62:63], 0, s[86:87]
	s_mov_b32 m0, s44
	v_lshl_add_u64 v[56:57], s[6:7], 0, v[56:57]
	global_load_lds_dwordx4 v[62:63], off
	v_lshl_add_u64 v[56:57], v[56:57], 0, s[88:89]
	s_add_i32 m0, s44, 0x8000
	v_mov_b32_e32 v59, v209
	global_load_lds_dwordx4 v[56:57], off
	v_lshl_add_u64 v[56:57], s[6:7], 0, v[58:59]
	v_lshlrev_b32_e32 v60, 1, v55
	v_lshl_add_u64 v[56:57], v[56:57], 0, s[86:87]
	s_add_i32 m0, s44, 0x400
	v_mov_b32_e32 v61, v209
	global_load_lds_dwordx4 v[56:57], off
	v_lshl_add_u64 v[56:57], s[6:7], 0, v[60:61]
	v_lshl_add_u64 v[56:57], v[56:57], 0, s[88:89]
	s_add_i32 m0, s44, 0x8400
	v_bfe_u32 v135, v128, 5, 1
	global_load_lds_dwordx4 v[56:57], off
	v_and_b32_e32 v235, 63, v128
	v_and_b32_e32 v131, 31, v128
	v_and_b32_e32 v136, 15, v128
	v_bfe_u32 v137, v128, 2, 2
	v_and_b32_e32 v139, 16, v128
	v_lshlrev_b32_e32 v140, 2, v128
	v_bitop3_b32 v128, v135, v128, 15 bitop3:0x78
	v_lshlrev_b32_e32 v240, 4, v128
	v_bitop3_b32 v128, v135, v136, 2 bitop3:0x36
	v_lshlrev_b32_e32 v241, 4, v128
	v_bitop3_b32 v128, v135, v136, 4 bitop3:0x36
	v_lshlrev_b32_e32 v242, 4, v128
	v_bitop3_b32 v128, v135, v136, 6 bitop3:0x36
	v_lshlrev_b32_e32 v243, 4, v128
	v_bitop3_b32 v128, v135, v136, 8 bitop3:0x36
	v_lshlrev_b32_e32 v244, 4, v128
	v_bitop3_b32 v128, v135, v136, 10 bitop3:0x36
	v_lshlrev_b32_e32 v245, 4, v128
	v_bitop3_b32 v128, v135, v136, 12 bitop3:0x36
	s_add_i32 s16, s38, s39
	v_lshlrev_b32_e32 v246, 4, v128
	v_bitop3_b32 v128, v135, v136, 14 bitop3:0x36
	v_or_b32_e32 v44, s38, v131
	s_add_i32 s40, s40, 0x10000
	v_lshl_add_u32 v237, v131, 8, 0
	v_lshlrev_b32_e32 v247, 4, v128
	v_lshlrev_b32_e32 v128, 4, v135
	v_add_lshl_u32 v131, s16, v131, 2
	v_add_u32_e32 v249, s40, v128
	v_sub_u32_e32 v128, v128, v131
	s_mulk_i32 s14, 0x6800
	v_add_u32_e32 v250, s97, v128
	v_mov_b32_e32 v128, s14
	v_mad_u32_u24 v128, v130, s96, v128
	v_or_b32_e32 v131, v128, v133
	s_addk_i32 s14, 0x3400
	v_lshlrev_b32_e32 v208, 1, v131
	v_mov_b32_e32 v131, s14
	v_mad_u32_u24 v130, v130, s96, v131
	v_or_b32_e32 v130, v130, v134
	s_ashr_i32 s17, s16, 31
	v_lshl_add_u64 v[210:211], s[8:9], 0, v[208:209]
	v_lshlrev_b32_e32 v208, 1, v130
	v_bitop3_b32 v128, v132, v128, v129 bitop3:0xde
	s_lshr_b32 s15, s39, 6
	s_lshr_b32 s17, s17, 26
	v_lshlrev_b32_e32 v138, 8, v137
	v_and_or_b32 v139, v140, 12, v139
	v_lshl_add_u64 v[216:217], s[8:9], 0, v[208:209]
	v_lshlrev_b32_e32 v208, 1, v128
	s_add_i32 s42, s15, 4
	s_add_i32 s17, s16, s17
	v_lshl_or_b32 v138, v135, 10, v138
	v_lshlrev_b32_e32 v139, 1, v139
	s_mul_i32 s15, s15, 0x68000
	v_lshl_add_u64 v[218:219], s[10:11], 0, v[208:209]
	v_add_u32_e32 v208, 0x6800, v208
	s_mov_b32 s41, 1
	v_lshl_add_u32 v236, v44, 8, s65
	s_mov_b32 s43, 0
	v_mov_b32_e32 v65, v64
	v_mov_b32_e32 v66, v64
	v_mov_b32_e32 v67, v64
	v_mov_b32_e32 v68, v64
	v_mov_b32_e32 v69, v64
	v_mov_b32_e32 v70, v64
	v_mov_b32_e32 v71, v64
	v_mov_b32_e32 v72, v64
	v_mov_b32_e32 v73, v64
	v_mov_b32_e32 v74, v64
	v_mov_b32_e32 v75, v64
	v_mov_b32_e32 v76, v64
	v_mov_b32_e32 v77, v64
	v_mov_b32_e32 v78, v64
	v_mov_b32_e32 v79, v64
	v_mov_b32_e32 v33, v32
	v_mov_b32_e32 v34, v32
	v_mov_b32_e32 v35, v32
	v_mov_b32_e32 v36, v32
	v_mov_b32_e32 v37, v32
	v_mov_b32_e32 v38, v32
	v_mov_b32_e32 v39, v32
	v_mov_b32_e32 v40, v32
	v_mov_b32_e32 v41, v32
	v_mov_b32_e32 v42, v32
	v_mov_b32_e32 v43, v32
	v_mov_b32_e32 v44, v32
	v_mov_b32_e32 v45, v32
	v_mov_b32_e32 v46, v32
	v_mov_b32_e32 v47, v32
	v_mov_b32_e32 v17, v16
	v_mov_b32_e32 v18, v16
	v_mov_b32_e32 v19, v16
	v_mov_b32_e32 v20, v16
	v_mov_b32_e32 v21, v16
	v_mov_b32_e32 v22, v16
	v_mov_b32_e32 v23, v16
	v_mov_b32_e32 v24, v16
	v_mov_b32_e32 v25, v16
	v_mov_b32_e32 v26, v16
	v_mov_b32_e32 v27, v16
	v_mov_b32_e32 v28, v16
	v_mov_b32_e32 v29, v16
	v_mov_b32_e32 v30, v16
	v_mov_b32_e32 v31, v16
	v_mov_b32_e32 v1, v0
	v_mov_b32_e32 v2, v0
	v_mov_b32_e32 v3, v0
	v_mov_b32_e32 v4, v0
	v_mov_b32_e32 v5, v0
	v_mov_b32_e32 v6, v0
	v_mov_b32_e32 v7, v0
	v_mov_b32_e32 v8, v0
	v_mov_b32_e32 v9, v0
	v_mov_b32_e32 v10, v0
	v_mov_b32_e32 v11, v0
	v_mov_b32_e32 v12, v0
	v_mov_b32_e32 v13, v0
	v_mov_b32_e32 v14, v0
	v_mov_b32_e32 v15, v0
	v_mov_b32_e32 v113, v112
	v_mov_b32_e32 v114, v112
	v_mov_b32_e32 v115, v112
	v_mov_b32_e32 v116, v112
	v_mov_b32_e32 v117, v112
	v_mov_b32_e32 v118, v112
	v_mov_b32_e32 v119, v112
	v_mov_b32_e32 v120, v112
	v_mov_b32_e32 v121, v112
	v_mov_b32_e32 v122, v112
	v_mov_b32_e32 v123, v112
	v_mov_b32_e32 v124, v112
	v_mov_b32_e32 v125, v112
	v_mov_b32_e32 v126, v112
	v_mov_b32_e32 v127, v112
	v_mov_b32_e32 v97, v96
	v_mov_b32_e32 v98, v96
	v_mov_b32_e32 v99, v96
	v_mov_b32_e32 v100, v96
	v_mov_b32_e32 v101, v96
	v_mov_b32_e32 v102, v96
	v_mov_b32_e32 v103, v96
	v_mov_b32_e32 v104, v96
	v_mov_b32_e32 v105, v96
	v_mov_b32_e32 v106, v96
	v_mov_b32_e32 v107, v96
	v_mov_b32_e32 v108, v96
	v_mov_b32_e32 v109, v96
	v_mov_b32_e32 v110, v96
	v_mov_b32_e32 v111, v96
	v_mov_b32_e32 v81, v80
	v_mov_b32_e32 v82, v80
	v_mov_b32_e32 v83, v80
	v_mov_b32_e32 v84, v80
	v_mov_b32_e32 v85, v80
	v_mov_b32_e32 v86, v80
	v_mov_b32_e32 v87, v80
	v_mov_b32_e32 v88, v80
	v_mov_b32_e32 v89, v80
	v_mov_b32_e32 v90, v80
	v_mov_b32_e32 v91, v80
	v_mov_b32_e32 v92, v80
	v_mov_b32_e32 v93, v80
	v_mov_b32_e32 v94, v80
	v_mov_b32_e32 v95, v80
	v_mov_b32_e32 v49, v48
	v_mov_b32_e32 v50, v48
	v_mov_b32_e32 v51, v48
	v_mov_b32_e32 v52, v48
	v_mov_b32_e32 v53, v48
	v_mov_b32_e32 v54, v48
	v_mov_b32_e32 v55, v48
	v_mov_b32_e32 v56, v48
	v_mov_b32_e32 v57, v48
	v_mov_b32_e32 v58, v48
	v_mov_b32_e32 v59, v48
	v_mov_b32_e32 v60, v48
	v_mov_b32_e32 v61, v48
	v_mov_b32_e32 v62, v48
	v_mov_b32_e32 v63, v48
	s_ashr_i32 s45, s17, 6
	v_add3_u32 v238, 0, v138, v139
	v_lshl_add_u32 v239, v235, 2, s40
	v_lshlrev_b32_e32 v248, 6, v137
	s_add_u32 s46, s15, 0x1a0000
	v_lshl_add_u64 v[220:221], s[10:11], 0, v[208:209]
	s_sub_i32 s47, 0, s16
	v_mov_b32_e32 v226, 0xff800000
	v_mov_b32_e32 v251, 0
	s_mov_b64 s[14:15], 0
	v_mov_b32_e32 v208, 0
	v_mov_b32_e32 v227, 0xff800000
	s_add_i32 m0, s44, 0x4000
	s_nop 0
	global_load_lds_dwordx4 v[210:211], off
	s_add_i32 m0, s44, 0x4400
	s_nop 0
	global_load_lds_dwordx4 v[216:217], off
	s_waitcnt vmcnt(0) lgkmcnt(0)
	s_barrier
	s_mov_b32 s48, 0
	v_mov_b32_e32 v228, s64
	ds_read_b32 v229, v228
	v_add3_u32 v254, v237, v240, s48
	ds_read_b128 v[128:131], v254
	ds_read_b128 v[132:135], v254 offset:8192
	v_add_u32_e32 v255, v236, v240
	ds_read_b128 v[136:139], v255
	v_add3_u32 v254, v237, v241, s48
	ds_read_b128 v[140:143], v254
	ds_read_b128 v[144:147], v254 offset:8192
	v_add_u32_e32 v255, v236, v241
	ds_read_b128 v[148:151], v255
	v_add3_u32 v254, v237, v242, s48
	ds_read_b128 v[152:155], v254
	ds_read_b128 v[156:159], v254 offset:8192
	v_add_u32_e32 v255, v236, v242
	ds_read_b128 v[192:195], v255
	v_add3_u32 v254, v237, v243, s48
	ds_read_b128 v[196:199], v254
	ds_read_b128 v[200:203], v254 offset:8192
	v_add_u32_e32 v255, v236, v243
	ds_read_b128 v[204:207], v255
	s_waitcnt lgkmcnt(9)
	v_mfma_f32_32x32x16_bf16 v[160:175], v[128:131], v[136:139], 0
	v_mfma_f32_32x32x16_bf16 v[176:191], v[132:135], v[136:139], 0
	s_waitcnt lgkmcnt(6)
	v_mfma_f32_32x32x16_bf16 v[160:175], v[140:143], v[148:151], v[160:175]
	v_mfma_f32_32x32x16_bf16 v[176:191], v[144:147], v[148:151], v[176:191]
	s_waitcnt lgkmcnt(3)
	v_mfma_f32_32x32x16_bf16 v[160:175], v[152:155], v[192:195], v[160:175]
	v_mfma_f32_32x32x16_bf16 v[176:191], v[156:159], v[192:195], v[176:191]
	s_waitcnt lgkmcnt(0)
	v_mfma_f32_32x32x16_bf16 v[160:175], v[196:199], v[204:207], v[160:175]
	v_mfma_f32_32x32x16_bf16 v[176:191], v[200:203], v[204:207], v[176:191]
	v_readfirstlane_b32 s50, v229
.Lattn_loop:
	s_add_i32 s16, s41, -1
	s_and_b32 s48, s43, 0x4000
	s_xor_b32 s51, s48, 0x4000
	s_cmpk_gt_i32 s47, 0xff66
	s_cselect_b32 s49, 0, s50
	s_sub_i32 s17, s16, s45
	s_cmp_gt_i32 s17, 1
	s_cbranch_scc1 .Lattn_mid
	s_cmp_eq_u32 s17, 1
	s_cbranch_scc1 .Lattn_s1drain
	s_cmp_eq_u32 s16, 0
	s_cbranch_scc1 .Lattn_s1first
	ds_read_b64_tr_b16 v[144:145], v212 offset:32768
	ds_read_b64_tr_b16 v[146:147], v212 offset:34816
	ds_read_b64_tr_b16 v[148:149], v213 offset:32768
	ds_read_b64_tr_b16 v[150:151], v213 offset:34816
	ds_read_b64_tr_b16 v[152:153], v214 offset:32768
	ds_read_b64_tr_b16 v[154:155], v214 offset:34816
	s_cmpk_gt_i32 s47, 0xff66
	s_cbranch_scc0 .Lattn_nobias0_a
	ds_read2_b32 v[192:193], v250 offset0:0 offset1:1
	ds_read2_b32 v[194:195], v250 offset0:2 offset1:3
	ds_read2_b32 v[196:197], v250 offset0:32 offset1:33
	ds_read2_b32 v[198:199], v250 offset0:34 offset1:35
	ds_read2_b32 v[200:201], v250 offset0:8 offset1:9
	ds_read2_b32 v[202:203], v250 offset0:10 offset1:11
	ds_read2_b32 v[204:205], v250 offset0:40 offset1:41
	ds_read2_b32 v[206:207], v250 offset0:42 offset1:43
	s_waitcnt lgkmcnt(7)
	v_add_f32_e32 v160, v160, v192
	v_add_f32_e32 v161, v161, v193
	s_waitcnt lgkmcnt(6)
	v_add_f32_e32 v162, v162, v194
	v_add_f32_e32 v163, v163, v195
	s_waitcnt lgkmcnt(5)
	v_add_f32_e32 v176, v176, v196
	v_add_f32_e32 v177, v177, v197
	s_waitcnt lgkmcnt(4)
	v_add_f32_e32 v178, v178, v198
	v_add_f32_e32 v179, v179, v199
	s_waitcnt lgkmcnt(3)
	v_add_f32_e32 v164, v164, v200
	v_add_f32_e32 v165, v165, v201
	s_waitcnt lgkmcnt(2)
	v_add_f32_e32 v166, v166, v202
	v_add_f32_e32 v167, v167, v203
	s_waitcnt lgkmcnt(1)
	v_add_f32_e32 v180, v180, v204
	v_add_f32_e32 v181, v181, v205
	s_waitcnt lgkmcnt(0)
	v_add_f32_e32 v182, v182, v206
	v_add_f32_e32 v183, v183, v207
	ds_read2_b32 v[192:193], v250 offset0:16 offset1:17
	ds_read2_b32 v[194:195], v250 offset0:18 offset1:19
	ds_read2_b32 v[196:197], v250 offset0:48 offset1:49
	ds_read2_b32 v[198:199], v250 offset0:50 offset1:51
	ds_read2_b32 v[200:201], v250 offset0:24 offset1:25
	ds_read2_b32 v[202:203], v250 offset0:26 offset1:27
	ds_read2_b32 v[204:205], v250 offset0:56 offset1:57
	ds_read2_b32 v[206:207], v250 offset0:58 offset1:59
	s_waitcnt lgkmcnt(7)
	v_add_f32_e32 v168, v168, v192
	v_add_f32_e32 v169, v169, v193
	s_waitcnt lgkmcnt(6)
	v_add_f32_e32 v170, v170, v194
	v_add_f32_e32 v171, v171, v195
	s_waitcnt lgkmcnt(5)
	v_add_f32_e32 v184, v184, v196
	v_add_f32_e32 v185, v185, v197
	s_waitcnt lgkmcnt(4)
	v_add_f32_e32 v186, v186, v198
	v_add_f32_e32 v187, v187, v199
	s_waitcnt lgkmcnt(3)
	v_add_f32_e32 v172, v172, v200
	v_add_f32_e32 v173, v173, v201
	s_waitcnt lgkmcnt(2)
	v_add_f32_e32 v174, v174, v202
	v_add_f32_e32 v175, v175, v203
	s_waitcnt lgkmcnt(1)
	v_add_f32_e32 v188, v188, v204
	v_add_f32_e32 v189, v189, v205
	s_waitcnt lgkmcnt(0)
	v_add_f32_e32 v190, v190, v206
	v_add_f32_e32 v191, v191, v207
.Lattn_nobias0_a:
	v_max3_f32 v228, v160, v161, v162
	v_max3_f32 v229, v163, v164, v165
	s_waitcnt lgkmcnt(4)
	v_mfma_f32_32x32x16_bf16 v[112:127], v[128:131], v[144:147], v[112:127]
	ds_read_b64_tr_b16 v[156:157], v215 offset:32768
	ds_read_b64_tr_b16 v[158:159], v215 offset:34816
	v_max3_f32 v228, v228, v166, v167
	v_max3_f32 v229, v229, v168, v169
	v_max3_f32 v228, v228, v170, v171
	v_max3_f32 v229, v229, v172, v173
	v_max3_f32 v228, v228, v174, v175
	v_max3_f32 v229, v229, v176, v177
	s_waitcnt lgkmcnt(4)
	v_mfma_f32_32x32x16_bf16 v[96:111], v[128:131], v[148:151], v[96:111]
	ds_read_b64_tr_b16 v[144:145], v212 offset:36864
	ds_read_b64_tr_b16 v[146:147], v212 offset:38912
	v_max3_f32 v228, v228, v178, v179
	v_max3_f32 v229, v229, v180, v181
	v_max3_f32 v228, v228, v182, v183
	v_max3_f32 v229, v229, v184, v185
	v_max3_f32 v228, v228, v186, v187
	v_max3_f32 v229, v229, v188, v189
	s_waitcnt lgkmcnt(4)
	v_mfma_f32_32x32x16_bf16 v[80:95], v[128:131], v[152:155], v[80:95]
	ds_read_b64_tr_b16 v[148:149], v213 offset:36864
	ds_read_b64_tr_b16 v[150:151], v213 offset:38912
	v_max3_f32 v228, v228, v190, v191
	v_max_f32_e32 v228, v228, v229
	v_mov_b32_e32 v229, v228
	s_nop 1
	v_permlane32_swap_b32_e32 v228, v229
	v_max_f32_e32 v228, v228, v229
	s_waitcnt lgkmcnt(4)
	v_mfma_f32_32x32x16_bf16 v[48:63], v[128:131], v[156:159], v[48:63]
	ds_read_b64_tr_b16 v[152:153], v214 offset:36864
	ds_read_b64_tr_b16 v[154:155], v214 offset:38912
	v_add_f32_e32 v228, s49, v228
	v_sub_f32_e32 v229, v228, v226
	v_cmp_lt_f32_e32 vcc, 0x41000000, v229
	s_nop 1
	v_cndmask_b32_e32 v229, v226, v228, vcc
	v_sub_f32_e32 v228, v226, v229
	v_exp_f32_e32 v228, v228
	v_mov_b32_e32 v226, v229
	v_subrev_f32_e32 v229, s49, v229
	v_cmp_neq_f32_e32 vcc, 1.0, v228
	s_cbranch_vccz .Lattn_noresc0_a
	ds_write_b32 v239, v228
	ds_read_b128 v[192:195], v249
	ds_read_b128 v[196:199], v249 offset:32
	ds_read_b128 v[200:203], v249 offset:64
	ds_read_b128 v[204:207], v249 offset:96
	s_waitcnt lgkmcnt(3)
	v_pk_mul_f32 v[64:65], v[64:65], v[192:193]
	v_pk_mul_f32 v[66:67], v[66:67], v[194:195]
	v_pk_mul_f32 v[32:33], v[32:33], v[192:193]
	v_pk_mul_f32 v[34:35], v[34:35], v[194:195]
	v_pk_mul_f32 v[16:17], v[16:17], v[192:193]
	v_pk_mul_f32 v[18:19], v[18:19], v[194:195]
	v_pk_mul_f32 v[0:1], v[0:1], v[192:193]
	v_pk_mul_f32 v[2:3], v[2:3], v[194:195]
	s_waitcnt lgkmcnt(2)
	v_pk_mul_f32 v[68:69], v[68:69], v[196:197]
	v_pk_mul_f32 v[70:71], v[70:71], v[198:199]
	v_pk_mul_f32 v[36:37], v[36:37], v[196:197]
	v_pk_mul_f32 v[38:39], v[38:39], v[198:199]
	v_pk_mul_f32 v[20:21], v[20:21], v[196:197]
	v_pk_mul_f32 v[22:23], v[22:23], v[198:199]
	v_pk_mul_f32 v[4:5], v[4:5], v[196:197]
	v_pk_mul_f32 v[6:7], v[6:7], v[198:199]
	s_waitcnt lgkmcnt(1)
	v_pk_mul_f32 v[72:73], v[72:73], v[200:201]
	v_pk_mul_f32 v[74:75], v[74:75], v[202:203]
	v_pk_mul_f32 v[40:41], v[40:41], v[200:201]
	v_pk_mul_f32 v[42:43], v[42:43], v[202:203]
	v_pk_mul_f32 v[24:25], v[24:25], v[200:201]
	v_pk_mul_f32 v[26:27], v[26:27], v[202:203]
	v_pk_mul_f32 v[8:9], v[8:9], v[200:201]
	v_pk_mul_f32 v[10:11], v[10:11], v[202:203]
	s_waitcnt lgkmcnt(0)
	v_pk_mul_f32 v[76:77], v[76:77], v[204:205]
	v_pk_mul_f32 v[78:79], v[78:79], v[206:207]
	v_pk_mul_f32 v[44:45], v[44:45], v[204:205]
	v_pk_mul_f32 v[46:47], v[46:47], v[206:207]
	v_pk_mul_f32 v[28:29], v[28:29], v[204:205]
	v_pk_mul_f32 v[30:31], v[30:31], v[206:207]
	v_pk_mul_f32 v[12:13], v[12:13], v[204:205]
	v_pk_mul_f32 v[14:15], v[14:15], v[206:207]
.Lattn_noresc0_a:
	ds_read_b64_tr_b16 v[156:157], v215 offset:36864
	ds_read_b64_tr_b16 v[158:159], v215 offset:38912
	ds_read_b64_tr_b16 v[192:193], v212 offset:40960
	ds_read_b64_tr_b16 v[194:195], v212 offset:43008
	ds_read_b64_tr_b16 v[196:197], v213 offset:40960
	ds_read_b64_tr_b16 v[198:199], v213 offset:43008
	ds_read_b64_tr_b16 v[200:201], v214 offset:40960
	ds_read_b64_tr_b16 v[202:203], v214 offset:43008
	v_sub_f32_e32 v160, v160, v229
	v_sub_f32_e32 v161, v161, v229
	v_sub_f32_e32 v162, v162, v229
	s_waitcnt lgkmcnt(12)
	v_mfma_f32_32x32x16_bf16 v[112:127], v[132:135], v[144:147], v[112:127]
	ds_read_b64_tr_b16 v[204:205], v215 offset:40960
	ds_read_b64_tr_b16 v[206:207], v215 offset:43008
	v_sub_f32_e32 v163, v163, v229
	v_exp_f32_e32 v160, v160
	v_exp_f32_e32 v161, v161
	v_exp_f32_e32 v162, v162
	v_exp_f32_e32 v163, v163
	s_waitcnt lgkmcnt(12)
	v_mfma_f32_32x32x16_bf16 v[96:111], v[132:135], v[148:151], v[96:111]
	ds_read_b64_tr_b16 v[144:145], v212 offset:45056
	ds_read_b64_tr_b16 v[146:147], v212 offset:47104
	v_add_f32_e32 v254, v160, v161
	v_add_f32_e32 v254, v254, v162
	v_add_f32_e32 v254, v254, v163
	v_sub_f32_e32 v164, v164, v229
	v_sub_f32_e32 v165, v165, v229
	s_waitcnt lgkmcnt(12)
	v_mfma_f32_32x32x16_bf16 v[80:95], v[132:135], v[152:155], v[80:95]
	ds_read_b64_tr_b16 v[148:149], v213 offset:45056
	ds_read_b64_tr_b16 v[150:151], v213 offset:47104
	v_sub_f32_e32 v166, v166, v229
	v_sub_f32_e32 v167, v167, v229
	v_exp_f32_e32 v164, v164
	v_exp_f32_e32 v165, v165
	v_exp_f32_e32 v166, v166
	s_waitcnt lgkmcnt(12)
	v_mfma_f32_32x32x16_bf16 v[48:63], v[132:135], v[156:159], v[48:63]
	ds_read_b64_tr_b16 v[152:153], v214 offset:45056
	ds_read_b64_tr_b16 v[154:155], v214 offset:47104
	v_exp_f32_e32 v167, v167
	v_add_f32_e32 v254, v254, v164
	v_add_f32_e32 v254, v254, v165
	v_add_f32_e32 v254, v254, v166
	v_add_f32_e32 v254, v254, v167
	s_waitcnt lgkmcnt(12)
	v_mfma_f32_32x32x16_bf16 v[112:127], v[136:139], v[192:195], v[112:127]
	ds_read_b64_tr_b16 v[156:157], v215 offset:45056
	ds_read_b64_tr_b16 v[158:159], v215 offset:47104
	v_cvt_pk_bf16_f32 v160, v160, v161
	v_cvt_pk_bf16_f32 v161, v162, v163
	v_sub_f32_e32 v168, v168, v229
	v_sub_f32_e32 v169, v169, v229
	v_sub_f32_e32 v170, v170, v229
	s_waitcnt lgkmcnt(12)
	v_mfma_f32_32x32x16_bf16 v[96:111], v[136:139], v[196:199], v[96:111]
	v_add_u32_e32 v230, v236, v244
	ds_read_b128 v[192:195], v230
	v_sub_f32_e32 v171, v171, v229
	v_exp_f32_e32 v168, v168
	v_exp_f32_e32 v169, v169
	v_exp_f32_e32 v170, v170
	v_exp_f32_e32 v171, v171
	s_waitcnt lgkmcnt(11)
	v_mfma_f32_32x32x16_bf16 v[80:95], v[136:139], v[200:203], v[80:95]
	v_add3_u32 v230, v237, v244, s48
	ds_read_b128 v[196:199], v230
	v_add_f32_e32 v254, v254, v168
	v_add_f32_e32 v254, v254, v169
	v_add_f32_e32 v254, v254, v170
	v_add_f32_e32 v254, v254, v171
	v_cvt_pk_bf16_f32 v162, v164, v165
	s_waitcnt lgkmcnt(10)
	v_mfma_f32_32x32x16_bf16 v[48:63], v[136:139], v[204:207], v[48:63]
	v_add3_u32 v230, v237, v244, s48
	ds_read_b128 v[200:203], v230 offset:8192
	v_cvt_pk_bf16_f32 v163, v166, v167
	v_sub_f32_e32 v172, v172, v229
	v_sub_f32_e32 v173, v173, v229
	v_sub_f32_e32 v174, v174, v229
	v_sub_f32_e32 v175, v175, v229
	s_waitcnt lgkmcnt(9)
	v_mfma_f32_32x32x16_bf16 v[112:127], v[140:143], v[144:147], v[112:127]
	v_add_u32_e32 v230, v236, v245
	ds_read_b128 v[204:207], v230
	v_exp_f32_e32 v172, v172
	v_exp_f32_e32 v173, v173
	v_exp_f32_e32 v174, v174
	v_exp_f32_e32 v175, v175
	v_add_f32_e32 v254, v254, v172
	s_waitcnt lgkmcnt(8)
	v_mfma_f32_32x32x16_bf16 v[96:111], v[140:143], v[148:151], v[96:111]
	v_add_f32_e32 v254, v254, v173
	v_add_f32_e32 v254, v254, v174
	v_add_f32_e32 v254, v254, v175
	v_cvt_pk_bf16_f32 v164, v168, v169
	v_cvt_pk_bf16_f32 v165, v170, v171
	s_waitcnt lgkmcnt(6)
	v_mfma_f32_32x32x16_bf16 v[80:95], v[140:143], v[152:155], v[80:95]
	v_sub_f32_e32 v176, v176, v229
	v_sub_f32_e32 v177, v177, v229
	v_sub_f32_e32 v178, v178, v229
	v_sub_f32_e32 v179, v179, v229
	v_exp_f32_e32 v176, v176
	v_exp_f32_e32 v177, v177
	s_waitcnt lgkmcnt(4)
	v_mfma_f32_32x32x16_bf16 v[48:63], v[140:143], v[156:159], v[48:63]
	v_exp_f32_e32 v178, v178
	v_exp_f32_e32 v179, v179
	v_add_f32_e32 v255, v176, v177
	v_add_f32_e32 v255, v255, v178
	v_add_f32_e32 v255, v255, v179
	s_waitcnt lgkmcnt(2)
	v_mfma_f32_32x32x16_bf16 v[128:143], v[196:199], v[192:195], 0
	v_add3_u32 v230, v237, v245, s48
	ds_read_b128 v[196:199], v230
	v_cvt_pk_bf16_f32 v166, v172, v173
	v_cvt_pk_bf16_f32 v167, v174, v175
	v_sub_f32_e32 v180, v180, v229
	v_sub_f32_e32 v181, v181, v229
	v_sub_f32_e32 v182, v182, v229
	s_waitcnt lgkmcnt(2)
	v_mfma_f32_32x32x16_bf16 v[144:159], v[200:203], v[192:195], 0
	v_add3_u32 v230, v237, v245, s48
	ds_read_b128 v[200:203], v230 offset:8192
	v_add_u32_e32 v230, v236, v246
	ds_read_b128 v[192:195], v230
	v_sub_f32_e32 v183, v183, v229
	v_exp_f32_e32 v180, v180
	v_exp_f32_e32 v181, v181
	v_exp_f32_e32 v182, v182
	v_exp_f32_e32 v183, v183
	s_waitcnt lgkmcnt(2)
	v_mfma_f32_32x32x16_bf16 v[128:143], v[196:199], v[204:207], v[128:143]
	v_add3_u32 v230, v237, v246, s48
	ds_read_b128 v[196:199], v230
	v_add_f32_e32 v255, v255, v180
	v_add_f32_e32 v255, v255, v181
	v_add_f32_e32 v255, v255, v182
	v_add_f32_e32 v255, v255, v183
	v_cvt_pk_bf16_f32 v168, v176, v177
	s_waitcnt lgkmcnt(2)
	v_mfma_f32_32x32x16_bf16 v[144:159], v[200:203], v[204:207], v[144:159]
	v_add3_u32 v230, v237, v246, s48
	ds_read_b128 v[200:203], v230 offset:8192
	v_add_u32_e32 v230, v236, v247
	ds_read_b128 v[204:207], v230
	v_cvt_pk_bf16_f32 v169, v178, v179
	v_sub_f32_e32 v184, v184, v229
	v_sub_f32_e32 v185, v185, v229
	v_sub_f32_e32 v186, v186, v229
	v_sub_f32_e32 v187, v187, v229
	s_waitcnt lgkmcnt(2)
	v_mfma_f32_32x32x16_bf16 v[128:143], v[196:199], v[192:195], v[128:143]
	v_add3_u32 v230, v237, v247, s48
	ds_read_b128 v[196:199], v230
	v_exp_f32_e32 v184, v184
	v_exp_f32_e32 v185, v185
	v_exp_f32_e32 v186, v186
	v_exp_f32_e32 v187, v187
	v_add_f32_e32 v255, v255, v184
	s_waitcnt lgkmcnt(2)
	v_mfma_f32_32x32x16_bf16 v[144:159], v[200:203], v[192:195], v[144:159]
	v_add3_u32 v230, v237, v247, s48
	ds_read_b128 v[200:203], v230 offset:8192
	v_add_f32_e32 v255, v255, v185
	v_add_f32_e32 v255, v255, v186
	v_add_f32_e32 v255, v255, v187
	v_cvt_pk_bf16_f32 v170, v180, v181
	v_cvt_pk_bf16_f32 v171, v182, v183
	s_waitcnt lgkmcnt(1)
	v_mfma_f32_32x32x16_bf16 v[128:143], v[196:199], v[204:207], v[128:143]
	v_sub_f32_e32 v188, v188, v229
	v_sub_f32_e32 v189, v189, v229
	v_sub_f32_e32 v190, v190, v229
	v_sub_f32_e32 v191, v191, v229
	v_exp_f32_e32 v188, v188
	s_waitcnt lgkmcnt(0)
	v_mfma_f32_32x32x16_bf16 v[144:159], v[200:203], v[204:207], v[144:159]
	v_exp_f32_e32 v189, v189
	v_exp_f32_e32 v190, v190
	v_exp_f32_e32 v191, v191
	v_add_f32_e32 v255, v255, v188
	v_add_f32_e32 v255, v255, v189
	v_add_f32_e32 v255, v255, v190
	v_add_f32_e32 v255, v255, v191
	v_cvt_pk_bf16_f32 v172, v184, v185
	v_cvt_pk_bf16_f32 v173, v186, v187
	v_cvt_pk_bf16_f32 v174, v188, v189
	v_cvt_pk_bf16_f32 v175, v190, v191
	v_add_f32_e32 v254, v254, v255
	v_mov_b32_e32 v255, v254
	s_nop 1
	v_permlane32_swap_b32_e32 v254, v255
	v_add_f32_e32 v254, v254, v255
	v_fma_f32 v251, v251, v228, v254
	s_branch .Lattn_mid
.Lattn_s1first:
	s_cmpk_gt_i32 s47, 0xff66
	s_cbranch_scc0 .Lattn_nobias0_b
	ds_read2_b32 v[192:193], v250 offset0:0 offset1:1
	ds_read2_b32 v[194:195], v250 offset0:2 offset1:3
	ds_read2_b32 v[196:197], v250 offset0:32 offset1:33
	ds_read2_b32 v[198:199], v250 offset0:34 offset1:35
	ds_read2_b32 v[200:201], v250 offset0:8 offset1:9
	ds_read2_b32 v[202:203], v250 offset0:10 offset1:11
	ds_read2_b32 v[204:205], v250 offset0:40 offset1:41
	ds_read2_b32 v[206:207], v250 offset0:42 offset1:43
	s_waitcnt lgkmcnt(7)
	v_add_f32_e32 v160, v160, v192
	v_add_f32_e32 v161, v161, v193
	s_waitcnt lgkmcnt(6)
	v_add_f32_e32 v162, v162, v194
	v_add_f32_e32 v163, v163, v195
	s_waitcnt lgkmcnt(5)
	v_add_f32_e32 v176, v176, v196
	v_add_f32_e32 v177, v177, v197
	s_waitcnt lgkmcnt(4)
	v_add_f32_e32 v178, v178, v198
	v_add_f32_e32 v179, v179, v199
	s_waitcnt lgkmcnt(3)
	v_add_f32_e32 v164, v164, v200
	v_add_f32_e32 v165, v165, v201
	s_waitcnt lgkmcnt(2)
	v_add_f32_e32 v166, v166, v202
	v_add_f32_e32 v167, v167, v203
	s_waitcnt lgkmcnt(1)
	v_add_f32_e32 v180, v180, v204
	v_add_f32_e32 v181, v181, v205
	s_waitcnt lgkmcnt(0)
	v_add_f32_e32 v182, v182, v206
	v_add_f32_e32 v183, v183, v207
	ds_read2_b32 v[192:193], v250 offset0:16 offset1:17
	ds_read2_b32 v[194:195], v250 offset0:18 offset1:19
	ds_read2_b32 v[196:197], v250 offset0:48 offset1:49
	ds_read2_b32 v[198:199], v250 offset0:50 offset1:51
	ds_read2_b32 v[200:201], v250 offset0:24 offset1:25
	ds_read2_b32 v[202:203], v250 offset0:26 offset1:27
	ds_read2_b32 v[204:205], v250 offset0:56 offset1:57
	ds_read2_b32 v[206:207], v250 offset0:58 offset1:59
	s_waitcnt lgkmcnt(7)
	v_add_f32_e32 v168, v168, v192
	v_add_f32_e32 v169, v169, v193
	s_waitcnt lgkmcnt(6)
	v_add_f32_e32 v170, v170, v194
	v_add_f32_e32 v171, v171, v195
	s_waitcnt lgkmcnt(5)
	v_add_f32_e32 v184, v184, v196
	v_add_f32_e32 v185, v185, v197
	s_waitcnt lgkmcnt(4)
	v_add_f32_e32 v186, v186, v198
	v_add_f32_e32 v187, v187, v199
	s_waitcnt lgkmcnt(3)
	v_add_f32_e32 v172, v172, v200
	v_add_f32_e32 v173, v173, v201
	s_waitcnt lgkmcnt(2)
	v_add_f32_e32 v174, v174, v202
	v_add_f32_e32 v175, v175, v203
	s_waitcnt lgkmcnt(1)
	v_add_f32_e32 v188, v188, v204
	v_add_f32_e32 v189, v189, v205
	s_waitcnt lgkmcnt(0)
	v_add_f32_e32 v190, v190, v206
	v_add_f32_e32 v191, v191, v207
.Lattn_nobias0_b:
	v_max3_f32 v228, v160, v161, v162
	v_max3_f32 v229, v163, v164, v165
	v_max3_f32 v228, v228, v166, v167
	v_max3_f32 v229, v229, v168, v169
	v_max3_f32 v228, v228, v170, v171
	v_max3_f32 v229, v229, v172, v173
	v_max3_f32 v228, v228, v174, v175
	v_max3_f32 v229, v229, v176, v177
	v_max3_f32 v228, v228, v178, v179
	v_max3_f32 v229, v229, v180, v181
	v_max3_f32 v228, v228, v182, v183
	v_max3_f32 v229, v229, v184, v185
	v_max3_f32 v228, v228, v186, v187
	v_max3_f32 v229, v229, v188, v189
	v_max3_f32 v228, v228, v190, v191
	v_max_f32_e32 v228, v228, v229
	v_mov_b32_e32 v229, v228
	s_nop 1
	v_permlane32_swap_b32_e32 v228, v229
	v_max_f32_e32 v228, v228, v229
	v_add_f32_e32 v228, s49, v228
	v_sub_f32_e32 v229, v228, v226
	v_cmp_lt_f32_e32 vcc, 0x41000000, v229
	s_nop 1
	v_cndmask_b32_e32 v229, v226, v228, vcc
	v_sub_f32_e32 v228, v226, v229
	v_exp_f32_e32 v228, v228
	v_mov_b32_e32 v226, v229
	v_subrev_f32_e32 v229, s49, v229
	v_cmp_neq_f32_e32 vcc, 1.0, v228
	s_cbranch_vccz .Lattn_noresc0_b
	ds_write_b32 v239, v228
	ds_read_b128 v[192:195], v249
	ds_read_b128 v[196:199], v249 offset:32
	ds_read_b128 v[200:203], v249 offset:64
	ds_read_b128 v[204:207], v249 offset:96
	s_waitcnt lgkmcnt(3)
	v_pk_mul_f32 v[64:65], v[64:65], v[192:193]
	v_pk_mul_f32 v[66:67], v[66:67], v[194:195]
	v_pk_mul_f32 v[32:33], v[32:33], v[192:193]
	v_pk_mul_f32 v[34:35], v[34:35], v[194:195]
	v_pk_mul_f32 v[16:17], v[16:17], v[192:193]
	v_pk_mul_f32 v[18:19], v[18:19], v[194:195]
	v_pk_mul_f32 v[0:1], v[0:1], v[192:193]
	v_pk_mul_f32 v[2:3], v[2:3], v[194:195]
	s_waitcnt lgkmcnt(2)
	v_pk_mul_f32 v[68:69], v[68:69], v[196:197]
	v_pk_mul_f32 v[70:71], v[70:71], v[198:199]
	v_pk_mul_f32 v[36:37], v[36:37], v[196:197]
	v_pk_mul_f32 v[38:39], v[38:39], v[198:199]
	v_pk_mul_f32 v[20:21], v[20:21], v[196:197]
	v_pk_mul_f32 v[22:23], v[22:23], v[198:199]
	v_pk_mul_f32 v[4:5], v[4:5], v[196:197]
	v_pk_mul_f32 v[6:7], v[6:7], v[198:199]
	s_waitcnt lgkmcnt(1)
	v_pk_mul_f32 v[72:73], v[72:73], v[200:201]
	v_pk_mul_f32 v[74:75], v[74:75], v[202:203]
	v_pk_mul_f32 v[40:41], v[40:41], v[200:201]
	v_pk_mul_f32 v[42:43], v[42:43], v[202:203]
	v_pk_mul_f32 v[24:25], v[24:25], v[200:201]
	v_pk_mul_f32 v[26:27], v[26:27], v[202:203]
	v_pk_mul_f32 v[8:9], v[8:9], v[200:201]
	v_pk_mul_f32 v[10:11], v[10:11], v[202:203]
	s_waitcnt lgkmcnt(0)
	v_pk_mul_f32 v[76:77], v[76:77], v[204:205]
	v_pk_mul_f32 v[78:79], v[78:79], v[206:207]
	v_pk_mul_f32 v[44:45], v[44:45], v[204:205]
	v_pk_mul_f32 v[46:47], v[46:47], v[206:207]
	v_pk_mul_f32 v[28:29], v[28:29], v[204:205]
	v_pk_mul_f32 v[30:31], v[30:31], v[206:207]
	v_pk_mul_f32 v[12:13], v[12:13], v[204:205]
	v_pk_mul_f32 v[14:15], v[14:15], v[206:207]
.Lattn_noresc0_b:
	v_add_u32_e32 v230, v236, v244
	ds_read_b128 v[192:195], v230
	v_add3_u32 v230, v237, v244, s48
	ds_read_b128 v[196:199], v230
	v_add3_u32 v230, v237, v244, s48
	ds_read_b128 v[200:203], v230 offset:8192
	v_add_u32_e32 v230, v236, v245
	ds_read_b128 v[204:207], v230
	v_sub_f32_e32 v160, v160, v229
	v_sub_f32_e32 v161, v161, v229
	v_sub_f32_e32 v162, v162, v229
	s_waitcnt lgkmcnt(2)
	v_mfma_f32_32x32x16_bf16 v[128:143], v[196:199], v[192:195], 0
	v_add3_u32 v230, v237, v245, s48
	ds_read_b128 v[196:199], v230
	v_sub_f32_e32 v163, v163, v229
	v_exp_f32_e32 v160, v160
	v_exp_f32_e32 v161, v161
	v_exp_f32_e32 v162, v162
	v_exp_f32_e32 v163, v163
	v_add_f32_e32 v254, v160, v161
	v_add_f32_e32 v254, v254, v162
	v_add_f32_e32 v254, v254, v163
	v_sub_f32_e32 v164, v164, v229
	v_sub_f32_e32 v165, v165, v229
	v_sub_f32_e32 v166, v166, v229
	v_sub_f32_e32 v167, v167, v229
	v_exp_f32_e32 v164, v164
	s_waitcnt lgkmcnt(2)
	v_mfma_f32_32x32x16_bf16 v[144:159], v[200:203], v[192:195], 0
	v_add3_u32 v230, v237, v245, s48
	ds_read_b128 v[200:203], v230 offset:8192
	v_add_u32_e32 v230, v236, v246
	ds_read_b128 v[192:195], v230
	v_exp_f32_e32 v165, v165
	v_exp_f32_e32 v166, v166
	v_exp_f32_e32 v167, v167
	v_add_f32_e32 v254, v254, v164
	v_add_f32_e32 v254, v254, v165
	v_add_f32_e32 v254, v254, v166
	v_add_f32_e32 v254, v254, v167
	v_cvt_pk_bf16_f32 v160, v160, v161
	v_cvt_pk_bf16_f32 v161, v162, v163
	v_sub_f32_e32 v168, v168, v229
	v_sub_f32_e32 v169, v169, v229
	v_sub_f32_e32 v170, v170, v229
	v_sub_f32_e32 v171, v171, v229
	v_exp_f32_e32 v168, v168
	s_waitcnt lgkmcnt(2)
	v_mfma_f32_32x32x16_bf16 v[128:143], v[196:199], v[204:207], v[128:143]
	v_add3_u32 v230, v237, v246, s48
	ds_read_b128 v[196:199], v230
	v_exp_f32_e32 v169, v169
	v_exp_f32_e32 v170, v170
	v_exp_f32_e32 v171, v171
	v_add_f32_e32 v254, v254, v168
	v_add_f32_e32 v254, v254, v169
	v_add_f32_e32 v254, v254, v170
	v_add_f32_e32 v254, v254, v171
	v_cvt_pk_bf16_f32 v162, v164, v165
	v_cvt_pk_bf16_f32 v163, v166, v167
	v_sub_f32_e32 v172, v172, v229
	v_sub_f32_e32 v173, v173, v229
	v_sub_f32_e32 v174, v174, v229
	v_sub_f32_e32 v175, v175, v229
	v_exp_f32_e32 v172, v172
	s_waitcnt lgkmcnt(2)
	v_mfma_f32_32x32x16_bf16 v[144:159], v[200:203], v[204:207], v[144:159]
	v_add3_u32 v230, v237, v246, s48
	ds_read_b128 v[200:203], v230 offset:8192
	v_add_u32_e32 v230, v236, v247
	ds_read_b128 v[204:207], v230
	v_exp_f32_e32 v173, v173
	v_exp_f32_e32 v174, v174
	v_exp_f32_e32 v175, v175
	v_add_f32_e32 v254, v254, v172
	v_add_f32_e32 v254, v254, v173
	v_add_f32_e32 v254, v254, v174
	v_add_f32_e32 v254, v254, v175
	v_cvt_pk_bf16_f32 v164, v168, v169
	v_cvt_pk_bf16_f32 v165, v170, v171
	v_sub_f32_e32 v176, v176, v229
	v_sub_f32_e32 v177, v177, v229
	v_sub_f32_e32 v178, v178, v229
	v_sub_f32_e32 v179, v179, v229
	v_exp_f32_e32 v176, v176
	s_waitcnt lgkmcnt(2)
	v_mfma_f32_32x32x16_bf16 v[128:143], v[196:199], v[192:195], v[128:143]
	v_add3_u32 v230, v237, v247, s48
	ds_read_b128 v[196:199], v230
	v_exp_f32_e32 v177, v177
	v_exp_f32_e32 v178, v178
	v_exp_f32_e32 v179, v179
	v_add_f32_e32 v255, v176, v177
	v_add_f32_e32 v255, v255, v178
	v_add_f32_e32 v255, v255, v179
	v_cvt_pk_bf16_f32 v166, v172, v173
	v_cvt_pk_bf16_f32 v167, v174, v175
	v_sub_f32_e32 v180, v180, v229
	v_sub_f32_e32 v181, v181, v229
	v_sub_f32_e32 v182, v182, v229
	v_sub_f32_e32 v183, v183, v229
	v_exp_f32_e32 v180, v180
	v_exp_f32_e32 v181, v181
	s_waitcnt lgkmcnt(2)
	v_mfma_f32_32x32x16_bf16 v[144:159], v[200:203], v[192:195], v[144:159]
	v_add3_u32 v230, v237, v247, s48
	ds_read_b128 v[200:203], v230 offset:8192
	v_exp_f32_e32 v182, v182
	v_exp_f32_e32 v183, v183
	v_add_f32_e32 v255, v255, v180
	v_add_f32_e32 v255, v255, v181
	v_add_f32_e32 v255, v255, v182
	v_add_f32_e32 v255, v255, v183
	v_cvt_pk_bf16_f32 v168, v176, v177
	v_cvt_pk_bf16_f32 v169, v178, v179
	v_sub_f32_e32 v184, v184, v229
	v_sub_f32_e32 v185, v185, v229
	v_sub_f32_e32 v186, v186, v229
	v_sub_f32_e32 v187, v187, v229
	v_exp_f32_e32 v184, v184
	s_waitcnt lgkmcnt(1)
	v_mfma_f32_32x32x16_bf16 v[128:143], v[196:199], v[204:207], v[128:143]
	v_exp_f32_e32 v185, v185
	v_exp_f32_e32 v186, v186
	v_exp_f32_e32 v187, v187
	v_add_f32_e32 v255, v255, v184
	v_add_f32_e32 v255, v255, v185
	v_add_f32_e32 v255, v255, v186
	v_add_f32_e32 v255, v255, v187
	v_cvt_pk_bf16_f32 v170, v180, v181
	v_cvt_pk_bf16_f32 v171, v182, v183
	v_sub_f32_e32 v188, v188, v229
	v_sub_f32_e32 v189, v189, v229
	v_sub_f32_e32 v190, v190, v229
	v_sub_f32_e32 v191, v191, v229
	v_exp_f32_e32 v188, v188
	s_waitcnt lgkmcnt(0)
	v_mfma_f32_32x32x16_bf16 v[144:159], v[200:203], v[204:207], v[144:159]
	v_exp_f32_e32 v189, v189
	v_exp_f32_e32 v190, v190
	v_exp_f32_e32 v191, v191
	v_add_f32_e32 v255, v255, v188
	v_add_f32_e32 v255, v255, v189
	v_add_f32_e32 v255, v255, v190
	v_add_f32_e32 v255, v255, v191
	v_cvt_pk_bf16_f32 v172, v184, v185
	v_cvt_pk_bf16_f32 v173, v186, v187
	v_cvt_pk_bf16_f32 v174, v188, v189
	v_cvt_pk_bf16_f32 v175, v190, v191
	v_add_f32_e32 v254, v254, v255
	v_mov_b32_e32 v255, v254
	s_nop 1
	v_permlane32_swap_b32_e32 v254, v255
	v_add_f32_e32 v254, v254, v255
	v_fma_f32 v251, v251, v228, v254
	s_branch .Lattn_mid
.Lattn_s1drain:
	ds_read_b64_tr_b16 v[192:193], v212 offset:32768
	ds_read_b64_tr_b16 v[194:195], v212 offset:34816
	ds_read_b64_tr_b16 v[196:197], v213 offset:32768
	ds_read_b64_tr_b16 v[198:199], v213 offset:34816
	ds_read_b64_tr_b16 v[200:201], v214 offset:32768
	ds_read_b64_tr_b16 v[202:203], v214 offset:34816
	ds_read_b64_tr_b16 v[204:205], v215 offset:32768
	ds_read_b64_tr_b16 v[206:207], v215 offset:34816
	ds_read_b64_tr_b16 v[144:145], v212 offset:36864
	ds_read_b64_tr_b16 v[146:147], v212 offset:38912
	ds_read_b64_tr_b16 v[148:149], v213 offset:36864
	ds_read_b64_tr_b16 v[150:151], v213 offset:38912
	ds_read_b64_tr_b16 v[152:153], v214 offset:36864
	ds_read_b64_tr_b16 v[154:155], v214 offset:38912
	s_waitcnt lgkmcnt(12)
	v_mfma_f32_32x32x16_bf16 v[112:127], v[128:131], v[192:195], v[112:127]
	ds_read_b64_tr_b16 v[156:157], v215 offset:36864
	ds_read_b64_tr_b16 v[158:159], v215 offset:38912
	s_waitcnt lgkmcnt(12)
	v_mfma_f32_32x32x16_bf16 v[96:111], v[128:131], v[196:199], v[96:111]
	ds_read_b64_tr_b16 v[160:161], v212 offset:40960
	ds_read_b64_tr_b16 v[162:163], v212 offset:43008
	s_waitcnt lgkmcnt(12)
	v_mfma_f32_32x32x16_bf16 v[80:95], v[128:131], v[200:203], v[80:95]
	ds_read_b64_tr_b16 v[164:165], v213 offset:40960
	ds_read_b64_tr_b16 v[166:167], v213 offset:43008
	s_waitcnt lgkmcnt(12)
	v_mfma_f32_32x32x16_bf16 v[48:63], v[128:131], v[204:207], v[48:63]
	ds_read_b64_tr_b16 v[168:169], v214 offset:40960
	ds_read_b64_tr_b16 v[170:171], v214 offset:43008
	s_waitcnt lgkmcnt(12)
	v_mfma_f32_32x32x16_bf16 v[112:127], v[132:135], v[144:147], v[112:127]
	ds_read_b64_tr_b16 v[172:173], v215 offset:40960
	ds_read_b64_tr_b16 v[174:175], v215 offset:43008
	s_waitcnt lgkmcnt(12)
	v_mfma_f32_32x32x16_bf16 v[96:111], v[132:135], v[148:151], v[96:111]
	ds_read_b64_tr_b16 v[176:177], v212 offset:45056
	ds_read_b64_tr_b16 v[178:179], v212 offset:47104
	s_waitcnt lgkmcnt(12)
	v_mfma_f32_32x32x16_bf16 v[80:95], v[132:135], v[152:155], v[80:95]
	ds_read_b64_tr_b16 v[180:181], v213 offset:45056
	ds_read_b64_tr_b16 v[182:183], v213 offset:47104
	s_waitcnt lgkmcnt(12)
	v_mfma_f32_32x32x16_bf16 v[48:63], v[132:135], v[156:159], v[48:63]
	ds_read_b64_tr_b16 v[184:185], v214 offset:45056
	ds_read_b64_tr_b16 v[186:187], v214 offset:47104
	s_waitcnt lgkmcnt(12)
	v_mfma_f32_32x32x16_bf16 v[112:127], v[136:139], v[160:163], v[112:127]
	ds_read_b64_tr_b16 v[188:189], v215 offset:45056
	ds_read_b64_tr_b16 v[190:191], v215 offset:47104
	s_waitcnt lgkmcnt(12)
	v_mfma_f32_32x32x16_bf16 v[96:111], v[136:139], v[164:167], v[96:111]
	s_waitcnt lgkmcnt(10)
	v_mfma_f32_32x32x16_bf16 v[80:95], v[136:139], v[168:171], v[80:95]
	s_waitcnt lgkmcnt(8)
	v_mfma_f32_32x32x16_bf16 v[48:63], v[136:139], v[172:175], v[48:63]
	s_waitcnt lgkmcnt(6)
	v_mfma_f32_32x32x16_bf16 v[112:127], v[140:143], v[176:179], v[112:127]
	s_waitcnt lgkmcnt(4)
	v_mfma_f32_32x32x16_bf16 v[96:111], v[140:143], v[180:183], v[96:111]
	s_waitcnt lgkmcnt(2)
	v_mfma_f32_32x32x16_bf16 v[80:95], v[140:143], v[184:187], v[80:95]
	s_waitcnt lgkmcnt(0)
	v_mfma_f32_32x32x16_bf16 v[48:63], v[140:143], v[188:191], v[48:63]
.Lattn_mid:
	s_waitcnt vmcnt(0) lgkmcnt(0)
	s_barrier
	s_add_i32 s17, s41, 1
	s_cmp_lt_u32 s17, s42
	s_cbranch_scc0 .Lattn_nok
	s_add_u32 s18, s14, 0x68000
	s_addc_u32 s19, s15, 0
	s_add_i32 s17, s44, s48
	v_lshl_add_u64 v[254:255], v[210:211], 0, s[18:19]
	s_mov_b32 m0, s17
	s_nop 0
	global_load_lds_dwordx4 v[254:255], off
	v_lshl_add_u64 v[254:255], v[216:217], 0, s[18:19]
	s_add_i32 m0, s17, 0x400
	s_nop 0
	global_load_lds_dwordx4 v[254:255], off
.Lattn_nok:
	s_cmp_lt_u32 s41, s42
	s_cbranch_scc0 .Lattn_nov
	s_add_i32 s17, s44, s51
	v_lshl_add_u64 v[254:255], v[218:219], 0, s[14:15]
	s_add_i32 m0, s17, 0x8000
	s_nop 0
	global_load_lds_dwordx4 v[254:255], off
	v_lshl_add_u64 v[254:255], v[220:221], 0, s[14:15]
	s_add_i32 m0, s17, 0x8400
	s_nop 0
	global_load_lds_dwordx4 v[254:255], off
.Lattn_nov:
	s_cmp_gt_i32 s16, s45
	s_cbranch_scc1 .Lattn_tail
	v_add3_u32 v212, v238, v248, s48
	v_xor_b32_e32 v228, 0x40, v248
	v_add3_u32 v213, v238, v228, s48
	v_xor_b32_e32 v228, 0x80, v248
	v_add3_u32 v214, v238, v228, s48
	v_xor_b32_e32 v228, 0xc0, v248
	v_add3_u32 v215, v238, v228, s48
	s_cmp_eq_u32 s16, s45
	s_cbranch_scc1 .Lattn_s2last
	ds_read_b64_tr_b16 v[176:177], v212 offset:32768
	ds_read_b64_tr_b16 v[178:179], v212 offset:34816
	ds_read_b64_tr_b16 v[180:181], v213 offset:32768
	ds_read_b64_tr_b16 v[182:183], v213 offset:34816
	ds_read_b64_tr_b16 v[184:185], v214 offset:32768
	ds_read_b64_tr_b16 v[186:187], v214 offset:34816
	s_cmpk_gt_i32 s47, 0xff66
	s_cbranch_scc0 .Lattn_nobias1_c
	ds_read2_b32 v[192:193], v250 offset0:0 offset1:1
	ds_read2_b32 v[194:195], v250 offset0:2 offset1:3
	ds_read2_b32 v[196:197], v250 offset0:32 offset1:33
	ds_read2_b32 v[198:199], v250 offset0:34 offset1:35
	ds_read2_b32 v[200:201], v250 offset0:8 offset1:9
	ds_read2_b32 v[202:203], v250 offset0:10 offset1:11
	ds_read2_b32 v[204:205], v250 offset0:40 offset1:41
	ds_read2_b32 v[206:207], v250 offset0:42 offset1:43
	s_waitcnt lgkmcnt(7)
	v_add_f32_e32 v128, v128, v192
	v_add_f32_e32 v129, v129, v193
	s_waitcnt lgkmcnt(6)
	v_add_f32_e32 v130, v130, v194
	v_add_f32_e32 v131, v131, v195
	s_waitcnt lgkmcnt(5)
	v_add_f32_e32 v144, v144, v196
	v_add_f32_e32 v145, v145, v197
	s_waitcnt lgkmcnt(4)
	v_add_f32_e32 v146, v146, v198
	v_add_f32_e32 v147, v147, v199
	s_waitcnt lgkmcnt(3)
	v_add_f32_e32 v132, v132, v200
	v_add_f32_e32 v133, v133, v201
	s_waitcnt lgkmcnt(2)
	v_add_f32_e32 v134, v134, v202
	v_add_f32_e32 v135, v135, v203
	s_waitcnt lgkmcnt(1)
	v_add_f32_e32 v148, v148, v204
	v_add_f32_e32 v149, v149, v205
	s_waitcnt lgkmcnt(0)
	v_add_f32_e32 v150, v150, v206
	v_add_f32_e32 v151, v151, v207
	ds_read2_b32 v[192:193], v250 offset0:16 offset1:17
	ds_read2_b32 v[194:195], v250 offset0:18 offset1:19
	ds_read2_b32 v[196:197], v250 offset0:48 offset1:49
	ds_read2_b32 v[198:199], v250 offset0:50 offset1:51
	ds_read2_b32 v[200:201], v250 offset0:24 offset1:25
	ds_read2_b32 v[202:203], v250 offset0:26 offset1:27
	ds_read2_b32 v[204:205], v250 offset0:56 offset1:57
	ds_read2_b32 v[206:207], v250 offset0:58 offset1:59
	s_waitcnt lgkmcnt(7)
	v_add_f32_e32 v136, v136, v192
	v_add_f32_e32 v137, v137, v193
	s_waitcnt lgkmcnt(6)
	v_add_f32_e32 v138, v138, v194
	v_add_f32_e32 v139, v139, v195
	s_waitcnt lgkmcnt(5)
	v_add_f32_e32 v152, v152, v196
	v_add_f32_e32 v153, v153, v197
	s_waitcnt lgkmcnt(4)
	v_add_f32_e32 v154, v154, v198
	v_add_f32_e32 v155, v155, v199
	s_waitcnt lgkmcnt(3)
	v_add_f32_e32 v140, v140, v200
	v_add_f32_e32 v141, v141, v201
	s_waitcnt lgkmcnt(2)
	v_add_f32_e32 v142, v142, v202
	v_add_f32_e32 v143, v143, v203
	s_waitcnt lgkmcnt(1)
	v_add_f32_e32 v156, v156, v204
	v_add_f32_e32 v157, v157, v205
	s_waitcnt lgkmcnt(0)
	v_add_f32_e32 v158, v158, v206
	v_add_f32_e32 v159, v159, v207
.Lattn_nobias1_c:
	v_max3_f32 v228, v128, v129, v130
	v_max3_f32 v229, v131, v132, v133
	s_waitcnt lgkmcnt(4)
	v_mfma_f32_32x32x16_bf16 v[64:79], v[160:163], v[176:179], v[64:79]
	ds_read_b64_tr_b16 v[188:189], v215 offset:32768
	ds_read_b64_tr_b16 v[190:191], v215 offset:34816
	v_max3_f32 v228, v228, v134, v135
	v_max3_f32 v229, v229, v136, v137
	v_max3_f32 v228, v228, v138, v139
	v_max3_f32 v229, v229, v140, v141
	v_max3_f32 v228, v228, v142, v143
	v_max3_f32 v229, v229, v144, v145
	s_waitcnt lgkmcnt(4)
	v_mfma_f32_32x32x16_bf16 v[32:47], v[160:163], v[180:183], v[32:47]
	ds_read_b64_tr_b16 v[176:177], v212 offset:36864
	ds_read_b64_tr_b16 v[178:179], v212 offset:38912
	v_max3_f32 v228, v228, v146, v147
	v_max3_f32 v229, v229, v148, v149
	v_max3_f32 v228, v228, v150, v151
	v_max3_f32 v229, v229, v152, v153
	v_max3_f32 v228, v228, v154, v155
	v_max3_f32 v229, v229, v156, v157
	s_waitcnt lgkmcnt(4)
	v_mfma_f32_32x32x16_bf16 v[16:31], v[160:163], v[184:187], v[16:31]
	ds_read_b64_tr_b16 v[180:181], v213 offset:36864
	ds_read_b64_tr_b16 v[182:183], v213 offset:38912
	v_max3_f32 v228, v228, v158, v159
	v_max_f32_e32 v228, v228, v229
	v_mov_b32_e32 v229, v228
	s_nop 1
	v_permlane32_swap_b32_e32 v228, v229
	v_max_f32_e32 v228, v228, v229
	s_waitcnt lgkmcnt(4)
	v_mfma_f32_32x32x16_bf16 v[0:15], v[160:163], v[188:191], v[0:15]
	ds_read_b64_tr_b16 v[184:185], v214 offset:36864
	ds_read_b64_tr_b16 v[186:187], v214 offset:38912
	v_add_f32_e32 v228, s49, v228
	v_sub_f32_e32 v229, v228, v227
	v_cmp_lt_f32_e32 vcc, 0x41000000, v229
	s_nop 1
	v_cndmask_b32_e32 v229, v227, v228, vcc
	v_sub_f32_e32 v228, v227, v229
	v_exp_f32_e32 v228, v228
	v_mov_b32_e32 v227, v229
	v_subrev_f32_e32 v229, s49, v229
	v_cmp_neq_f32_e32 vcc, 1.0, v228
	s_cbranch_vccz .Lattn_noresc1_c
	ds_write_b32 v239, v228
	ds_read_b128 v[192:195], v249
	ds_read_b128 v[196:199], v249 offset:32
	ds_read_b128 v[200:203], v249 offset:64
	ds_read_b128 v[204:207], v249 offset:96
	s_waitcnt lgkmcnt(3)
	v_pk_mul_f32 v[112:113], v[112:113], v[192:193]
	v_pk_mul_f32 v[114:115], v[114:115], v[194:195]
	v_pk_mul_f32 v[96:97], v[96:97], v[192:193]
	v_pk_mul_f32 v[98:99], v[98:99], v[194:195]
	v_pk_mul_f32 v[80:81], v[80:81], v[192:193]
	v_pk_mul_f32 v[82:83], v[82:83], v[194:195]
	v_pk_mul_f32 v[48:49], v[48:49], v[192:193]
	v_pk_mul_f32 v[50:51], v[50:51], v[194:195]
	s_waitcnt lgkmcnt(2)
	v_pk_mul_f32 v[116:117], v[116:117], v[196:197]
	v_pk_mul_f32 v[118:119], v[118:119], v[198:199]
	v_pk_mul_f32 v[100:101], v[100:101], v[196:197]
	v_pk_mul_f32 v[102:103], v[102:103], v[198:199]
	v_pk_mul_f32 v[84:85], v[84:85], v[196:197]
	v_pk_mul_f32 v[86:87], v[86:87], v[198:199]
	v_pk_mul_f32 v[52:53], v[52:53], v[196:197]
	v_pk_mul_f32 v[54:55], v[54:55], v[198:199]
	s_waitcnt lgkmcnt(1)
	v_pk_mul_f32 v[120:121], v[120:121], v[200:201]
	v_pk_mul_f32 v[122:123], v[122:123], v[202:203]
	v_pk_mul_f32 v[104:105], v[104:105], v[200:201]
	v_pk_mul_f32 v[106:107], v[106:107], v[202:203]
	v_pk_mul_f32 v[88:89], v[88:89], v[200:201]
	v_pk_mul_f32 v[90:91], v[90:91], v[202:203]
	v_pk_mul_f32 v[56:57], v[56:57], v[200:201]
	v_pk_mul_f32 v[58:59], v[58:59], v[202:203]
	s_waitcnt lgkmcnt(0)
	v_pk_mul_f32 v[124:125], v[124:125], v[204:205]
	v_pk_mul_f32 v[126:127], v[126:127], v[206:207]
	v_pk_mul_f32 v[108:109], v[108:109], v[204:205]
	v_pk_mul_f32 v[110:111], v[110:111], v[206:207]
	v_pk_mul_f32 v[92:93], v[92:93], v[204:205]
	v_pk_mul_f32 v[94:95], v[94:95], v[206:207]
	v_pk_mul_f32 v[60:61], v[60:61], v[204:205]
	v_pk_mul_f32 v[62:63], v[62:63], v[206:207]
.Lattn_noresc1_c:
	ds_read_b64_tr_b16 v[188:189], v215 offset:36864
	ds_read_b64_tr_b16 v[190:191], v215 offset:38912
	ds_read_b64_tr_b16 v[192:193], v212 offset:40960
	ds_read_b64_tr_b16 v[194:195], v212 offset:43008
	ds_read_b64_tr_b16 v[196:197], v213 offset:40960
	ds_read_b64_tr_b16 v[198:199], v213 offset:43008
	ds_read_b64_tr_b16 v[200:201], v214 offset:40960
	ds_read_b64_tr_b16 v[202:203], v214 offset:43008
	v_sub_f32_e32 v128, v128, v229
	v_sub_f32_e32 v129, v129, v229
	v_sub_f32_e32 v130, v130, v229
	s_waitcnt lgkmcnt(12)
	v_mfma_f32_32x32x16_bf16 v[64:79], v[164:167], v[176:179], v[64:79]
	ds_read_b64_tr_b16 v[204:205], v215 offset:40960
	ds_read_b64_tr_b16 v[206:207], v215 offset:43008
	v_sub_f32_e32 v131, v131, v229
	v_exp_f32_e32 v128, v128
	v_exp_f32_e32 v129, v129
	v_exp_f32_e32 v130, v130
	v_exp_f32_e32 v131, v131
	s_waitcnt lgkmcnt(12)
	v_mfma_f32_32x32x16_bf16 v[32:47], v[164:167], v[180:183], v[32:47]
	ds_read_b64_tr_b16 v[176:177], v212 offset:45056
	ds_read_b64_tr_b16 v[178:179], v212 offset:47104
	v_add_f32_e32 v254, v128, v129
	v_add_f32_e32 v254, v254, v130
	v_add_f32_e32 v254, v254, v131
	v_sub_f32_e32 v132, v132, v229
	v_sub_f32_e32 v133, v133, v229
	s_waitcnt lgkmcnt(12)
	v_mfma_f32_32x32x16_bf16 v[16:31], v[164:167], v[184:187], v[16:31]
	ds_read_b64_tr_b16 v[180:181], v213 offset:45056
	ds_read_b64_tr_b16 v[182:183], v213 offset:47104
	v_sub_f32_e32 v134, v134, v229
	v_sub_f32_e32 v135, v135, v229
	v_exp_f32_e32 v132, v132
	v_exp_f32_e32 v133, v133
	v_exp_f32_e32 v134, v134
	s_waitcnt lgkmcnt(12)
	v_mfma_f32_32x32x16_bf16 v[0:15], v[164:167], v[188:191], v[0:15]
	ds_read_b64_tr_b16 v[184:185], v214 offset:45056
	ds_read_b64_tr_b16 v[186:187], v214 offset:47104
	v_exp_f32_e32 v135, v135
	v_add_f32_e32 v254, v254, v132
	v_add_f32_e32 v254, v254, v133
	v_add_f32_e32 v254, v254, v134
	v_add_f32_e32 v254, v254, v135
	s_waitcnt lgkmcnt(12)
	v_mfma_f32_32x32x16_bf16 v[64:79], v[168:171], v[192:195], v[64:79]
	ds_read_b64_tr_b16 v[188:189], v215 offset:45056
	ds_read_b64_tr_b16 v[190:191], v215 offset:47104
	v_cvt_pk_bf16_f32 v128, v128, v129
	v_cvt_pk_bf16_f32 v129, v130, v131
	v_sub_f32_e32 v136, v136, v229
	v_sub_f32_e32 v137, v137, v229
	v_sub_f32_e32 v138, v138, v229
	s_waitcnt lgkmcnt(12)
	v_mfma_f32_32x32x16_bf16 v[32:47], v[168:171], v[196:199], v[32:47]
	v_add_u32_e32 v230, v236, v240
	ds_read_b128 v[192:195], v230
	v_sub_f32_e32 v139, v139, v229
	v_exp_f32_e32 v136, v136
	v_exp_f32_e32 v137, v137
	v_exp_f32_e32 v138, v138
	v_exp_f32_e32 v139, v139
	s_waitcnt lgkmcnt(11)
	v_mfma_f32_32x32x16_bf16 v[16:31], v[168:171], v[200:203], v[16:31]
	v_add3_u32 v230, v237, v240, s51
	ds_read_b128 v[196:199], v230
	v_add_f32_e32 v254, v254, v136
	v_add_f32_e32 v254, v254, v137
	v_add_f32_e32 v254, v254, v138
	v_add_f32_e32 v254, v254, v139
	v_cvt_pk_bf16_f32 v130, v132, v133
	s_waitcnt lgkmcnt(10)
	v_mfma_f32_32x32x16_bf16 v[0:15], v[168:171], v[204:207], v[0:15]
	v_add3_u32 v230, v237, v240, s51
	ds_read_b128 v[200:203], v230 offset:8192
	v_cvt_pk_bf16_f32 v131, v134, v135
	v_sub_f32_e32 v140, v140, v229
	v_sub_f32_e32 v141, v141, v229
	v_sub_f32_e32 v142, v142, v229
	v_sub_f32_e32 v143, v143, v229
	s_waitcnt lgkmcnt(9)
	v_mfma_f32_32x32x16_bf16 v[64:79], v[172:175], v[176:179], v[64:79]
	v_add_u32_e32 v230, v236, v241
	ds_read_b128 v[204:207], v230
	v_exp_f32_e32 v140, v140
	v_exp_f32_e32 v141, v141
	v_exp_f32_e32 v142, v142
	v_exp_f32_e32 v143, v143
	v_add_f32_e32 v254, v254, v140
	s_waitcnt lgkmcnt(8)
	v_mfma_f32_32x32x16_bf16 v[32:47], v[172:175], v[180:183], v[32:47]
	v_add_f32_e32 v254, v254, v141
	v_add_f32_e32 v254, v254, v142
	v_add_f32_e32 v254, v254, v143
	v_cvt_pk_bf16_f32 v132, v136, v137
	v_cvt_pk_bf16_f32 v133, v138, v139
	s_waitcnt lgkmcnt(6)
	v_mfma_f32_32x32x16_bf16 v[16:31], v[172:175], v[184:187], v[16:31]
	v_sub_f32_e32 v144, v144, v229
	v_sub_f32_e32 v145, v145, v229
	v_sub_f32_e32 v146, v146, v229
	v_sub_f32_e32 v147, v147, v229
	v_exp_f32_e32 v144, v144
	v_exp_f32_e32 v145, v145
	s_waitcnt lgkmcnt(4)
	v_mfma_f32_32x32x16_bf16 v[0:15], v[172:175], v[188:191], v[0:15]
	v_exp_f32_e32 v146, v146
	v_exp_f32_e32 v147, v147
	v_add_f32_e32 v255, v144, v145
	v_add_f32_e32 v255, v255, v146
	v_add_f32_e32 v255, v255, v147
	s_waitcnt lgkmcnt(2)
	v_mfma_f32_32x32x16_bf16 v[160:175], v[196:199], v[192:195], 0
	v_add3_u32 v230, v237, v241, s51
	ds_read_b128 v[196:199], v230
	v_cvt_pk_bf16_f32 v134, v140, v141
	v_cvt_pk_bf16_f32 v135, v142, v143
	v_sub_f32_e32 v148, v148, v229
	v_sub_f32_e32 v149, v149, v229
	v_sub_f32_e32 v150, v150, v229
	s_waitcnt lgkmcnt(2)
	v_mfma_f32_32x32x16_bf16 v[176:191], v[200:203], v[192:195], 0
	v_add3_u32 v230, v237, v241, s51
	ds_read_b128 v[200:203], v230 offset:8192
	v_add_u32_e32 v230, v236, v242
	ds_read_b128 v[192:195], v230
	v_sub_f32_e32 v151, v151, v229
	v_exp_f32_e32 v148, v148
	v_exp_f32_e32 v149, v149
	v_exp_f32_e32 v150, v150
	v_exp_f32_e32 v151, v151
	s_waitcnt lgkmcnt(2)
	v_mfma_f32_32x32x16_bf16 v[160:175], v[196:199], v[204:207], v[160:175]
	v_add3_u32 v230, v237, v242, s51
	ds_read_b128 v[196:199], v230
	v_add_f32_e32 v255, v255, v148
	v_add_f32_e32 v255, v255, v149
	v_add_f32_e32 v255, v255, v150
	v_add_f32_e32 v255, v255, v151
	v_cvt_pk_bf16_f32 v136, v144, v145
	s_waitcnt lgkmcnt(2)
	v_mfma_f32_32x32x16_bf16 v[176:191], v[200:203], v[204:207], v[176:191]
	v_add3_u32 v230, v237, v242, s51
	ds_read_b128 v[200:203], v230 offset:8192
	v_add_u32_e32 v230, v236, v243
	ds_read_b128 v[204:207], v230
	v_cvt_pk_bf16_f32 v137, v146, v147
	v_sub_f32_e32 v152, v152, v229
	v_sub_f32_e32 v153, v153, v229
	v_sub_f32_e32 v154, v154, v229
	v_sub_f32_e32 v155, v155, v229
	s_waitcnt lgkmcnt(2)
	v_mfma_f32_32x32x16_bf16 v[160:175], v[196:199], v[192:195], v[160:175]
	v_add3_u32 v230, v237, v243, s51
	ds_read_b128 v[196:199], v230
	v_exp_f32_e32 v152, v152
	v_exp_f32_e32 v153, v153
	v_exp_f32_e32 v154, v154
	v_exp_f32_e32 v155, v155
	v_add_f32_e32 v255, v255, v152
	s_waitcnt lgkmcnt(2)
	v_mfma_f32_32x32x16_bf16 v[176:191], v[200:203], v[192:195], v[176:191]
	v_add3_u32 v230, v237, v243, s51
	ds_read_b128 v[200:203], v230 offset:8192
	v_add_f32_e32 v255, v255, v153
	v_add_f32_e32 v255, v255, v154
	v_add_f32_e32 v255, v255, v155
	v_cvt_pk_bf16_f32 v138, v148, v149
	v_cvt_pk_bf16_f32 v139, v150, v151
	s_waitcnt lgkmcnt(1)
	v_mfma_f32_32x32x16_bf16 v[160:175], v[196:199], v[204:207], v[160:175]
	v_sub_f32_e32 v156, v156, v229
	v_sub_f32_e32 v157, v157, v229
	v_sub_f32_e32 v158, v158, v229
	v_sub_f32_e32 v159, v159, v229
	v_exp_f32_e32 v156, v156
	s_waitcnt lgkmcnt(0)
	v_mfma_f32_32x32x16_bf16 v[176:191], v[200:203], v[204:207], v[176:191]
	v_exp_f32_e32 v157, v157
	v_exp_f32_e32 v158, v158
	v_exp_f32_e32 v159, v159
	v_add_f32_e32 v255, v255, v156
	v_add_f32_e32 v255, v255, v157
	v_add_f32_e32 v255, v255, v158
	v_add_f32_e32 v255, v255, v159
	v_cvt_pk_bf16_f32 v140, v152, v153
	v_cvt_pk_bf16_f32 v141, v154, v155
	v_cvt_pk_bf16_f32 v142, v156, v157
	v_cvt_pk_bf16_f32 v143, v158, v159
	v_add_f32_e32 v254, v254, v255
	v_mov_b32_e32 v255, v254
	s_nop 1
	v_permlane32_swap_b32_e32 v254, v255
	v_add_f32_e32 v254, v254, v255
	v_fma_f32 v208, v208, v228, v254
	s_branch .Lattn_tail
.Lattn_s2last:
	ds_read_b64_tr_b16 v[176:177], v212 offset:32768
	ds_read_b64_tr_b16 v[178:179], v212 offset:34816
	ds_read_b64_tr_b16 v[180:181], v213 offset:32768
	ds_read_b64_tr_b16 v[182:183], v213 offset:34816
	ds_read_b64_tr_b16 v[184:185], v214 offset:32768
	ds_read_b64_tr_b16 v[186:187], v214 offset:34816
	s_cmpk_gt_i32 s47, 0xff66
	s_cbranch_scc0 .Lattn_nobias1_d
	ds_read2_b32 v[192:193], v250 offset0:0 offset1:1
	ds_read2_b32 v[194:195], v250 offset0:2 offset1:3
	ds_read2_b32 v[196:197], v250 offset0:32 offset1:33
	ds_read2_b32 v[198:199], v250 offset0:34 offset1:35
	ds_read2_b32 v[200:201], v250 offset0:8 offset1:9
	ds_read2_b32 v[202:203], v250 offset0:10 offset1:11
	ds_read2_b32 v[204:205], v250 offset0:40 offset1:41
	ds_read2_b32 v[206:207], v250 offset0:42 offset1:43
	s_waitcnt lgkmcnt(7)
	v_add_f32_e32 v128, v128, v192
	v_add_f32_e32 v129, v129, v193
	s_waitcnt lgkmcnt(6)
	v_add_f32_e32 v130, v130, v194
	v_add_f32_e32 v131, v131, v195
	s_waitcnt lgkmcnt(5)
	v_add_f32_e32 v144, v144, v196
	v_add_f32_e32 v145, v145, v197
	s_waitcnt lgkmcnt(4)
	v_add_f32_e32 v146, v146, v198
	v_add_f32_e32 v147, v147, v199
	s_waitcnt lgkmcnt(3)
	v_add_f32_e32 v132, v132, v200
	v_add_f32_e32 v133, v133, v201
	s_waitcnt lgkmcnt(2)
	v_add_f32_e32 v134, v134, v202
	v_add_f32_e32 v135, v135, v203
	s_waitcnt lgkmcnt(1)
	v_add_f32_e32 v148, v148, v204
	v_add_f32_e32 v149, v149, v205
	s_waitcnt lgkmcnt(0)
	v_add_f32_e32 v150, v150, v206
	v_add_f32_e32 v151, v151, v207
	ds_read2_b32 v[192:193], v250 offset0:16 offset1:17
	ds_read2_b32 v[194:195], v250 offset0:18 offset1:19
	ds_read2_b32 v[196:197], v250 offset0:48 offset1:49
	ds_read2_b32 v[198:199], v250 offset0:50 offset1:51
	ds_read2_b32 v[200:201], v250 offset0:24 offset1:25
	ds_read2_b32 v[202:203], v250 offset0:26 offset1:27
	ds_read2_b32 v[204:205], v250 offset0:56 offset1:57
	ds_read2_b32 v[206:207], v250 offset0:58 offset1:59
	s_waitcnt lgkmcnt(7)
	v_add_f32_e32 v136, v136, v192
	v_add_f32_e32 v137, v137, v193
	s_waitcnt lgkmcnt(6)
	v_add_f32_e32 v138, v138, v194
	v_add_f32_e32 v139, v139, v195
	s_waitcnt lgkmcnt(5)
	v_add_f32_e32 v152, v152, v196
	v_add_f32_e32 v153, v153, v197
	s_waitcnt lgkmcnt(4)
	v_add_f32_e32 v154, v154, v198
	v_add_f32_e32 v155, v155, v199
	s_waitcnt lgkmcnt(3)
	v_add_f32_e32 v140, v140, v200
	v_add_f32_e32 v141, v141, v201
	s_waitcnt lgkmcnt(2)
	v_add_f32_e32 v142, v142, v202
	v_add_f32_e32 v143, v143, v203
	s_waitcnt lgkmcnt(1)
	v_add_f32_e32 v156, v156, v204
	v_add_f32_e32 v157, v157, v205
	s_waitcnt lgkmcnt(0)
	v_add_f32_e32 v158, v158, v206
	v_add_f32_e32 v159, v159, v207

.Lattn_noresc1_d:
	ds_read_b64_tr_b16 v[188:189], v215 offset:36864
	ds_read_b64_tr_b16 v[190:191], v215 offset:38912
	ds_read_b64_tr_b16 v[192:193], v212 offset:40960
	ds_read_b64_tr_b16 v[194:195], v212 offset:43008
	ds_read_b64_tr_b16 v[196:197], v213 offset:40960
	ds_read_b64_tr_b16 v[198:199], v213 offset:43008
	ds_read_b64_tr_b16 v[200:201], v214 offset:40960
	ds_read_b64_tr_b16 v[202:203], v214 offset:43008
	v_sub_f32_e32 v128, v128, v229
	v_sub_f32_e32 v129, v129, v229
	v_sub_f32_e32 v130, v130, v229
	s_waitcnt lgkmcnt(12)
	v_mfma_f32_32x32x16_bf16 v[64:79], v[164:167], v[176:179], v[64:79]
	ds_read_b64_tr_b16 v[204:205], v215 offset:40960
	ds_read_b64_tr_b16 v[206:207], v215 offset:43008
	v_sub_f32_e32 v131, v131, v229
	v_exp_f32_e32 v128, v128
	v_exp_f32_e32 v129, v129
	v_exp_f32_e32 v130, v130
	v_exp_f32_e32 v131, v131
	v_add_f32_e32 v254, v128, v129
	v_add_f32_e32 v254, v254, v130
	v_add_f32_e32 v254, v254, v131
	s_waitcnt lgkmcnt(12)
	v_mfma_f32_32x32x16_bf16 v[32:47], v[164:167], v[180:183], v[32:47]
	ds_read_b64_tr_b16 v[176:177], v212 offset:45056
	ds_read_b64_tr_b16 v[178:179], v212 offset:47104
	v_sub_f32_e32 v132, v132, v229
	v_sub_f32_e32 v133, v133, v229
	v_sub_f32_e32 v134, v134, v229
	v_sub_f32_e32 v135, v135, v229
	v_exp_f32_e32 v132, v132
	v_exp_f32_e32 v133, v133
	v_exp_f32_e32 v134, v134
	v_exp_f32_e32 v135, v135
	v_add_f32_e32 v254, v254, v132
	s_waitcnt lgkmcnt(12)
	v_mfma_f32_32x32x16_bf16 v[16:31], v[164:167], v[184:187], v[16:31]
	ds_read_b64_tr_b16 v[180:181], v213 offset:45056
	ds_read_b64_tr_b16 v[182:183], v213 offset:47104
	v_add_f32_e32 v254, v254, v133
	v_add_f32_e32 v254, v254, v134
	v_add_f32_e32 v254, v254, v135
	v_cvt_pk_bf16_f32 v128, v128, v129
	v_cvt_pk_bf16_f32 v129, v130, v131
	v_sub_f32_e32 v136, v136, v229
	v_sub_f32_e32 v137, v137, v229
	v_sub_f32_e32 v138, v138, v229
	v_sub_f32_e32 v139, v139, v229
	s_waitcnt lgkmcnt(12)
	v_mfma_f32_32x32x16_bf16 v[0:15], v[164:167], v[188:191], v[0:15]
	ds_read_b64_tr_b16 v[184:185], v214 offset:45056
	ds_read_b64_tr_b16 v[186:187], v214 offset:47104
	v_exp_f32_e32 v136, v136
	v_exp_f32_e32 v137, v137
	v_exp_f32_e32 v138, v138
	v_exp_f32_e32 v139, v139
	v_add_f32_e32 v254, v254, v136
	v_add_f32_e32 v254, v254, v137
	v_add_f32_e32 v254, v254, v138
	v_add_f32_e32 v254, v254, v139
	v_cvt_pk_bf16_f32 v130, v132, v133
	s_waitcnt lgkmcnt(12)
	v_mfma_f32_32x32x16_bf16 v[64:79], v[168:171], v[192:195], v[64:79]
	ds_read_b64_tr_b16 v[188:189], v215 offset:45056
	ds_read_b64_tr_b16 v[190:191], v215 offset:47104
	v_cvt_pk_bf16_f32 v131, v134, v135
	v_sub_f32_e32 v140, v140, v229
	v_sub_f32_e32 v141, v141, v229
	v_sub_f32_e32 v142, v142, v229
	v_sub_f32_e32 v143, v143, v229
	v_exp_f32_e32 v140, v140
	v_exp_f32_e32 v141, v141
	v_exp_f32_e32 v142, v142
	s_waitcnt lgkmcnt(12)
	v_mfma_f32_32x32x16_bf16 v[32:47], v[168:171], v[196:199], v[32:47]
	v_exp_f32_e32 v143, v143
	v_add_f32_e32 v254, v254, v140
	v_add_f32_e32 v254, v254, v141
	v_add_f32_e32 v254, v254, v142
	v_add_f32_e32 v254, v254, v143
	v_cvt_pk_bf16_f32 v132, v136, v137
	v_cvt_pk_bf16_f32 v133, v138, v139
	v_sub_f32_e32 v144, v144, v229
	v_sub_f32_e32 v145, v145, v229
	s_waitcnt lgkmcnt(10)
	v_mfma_f32_32x32x16_bf16 v[16:31], v[168:171], v[200:203], v[16:31]
	v_sub_f32_e32 v146, v146, v229
	v_sub_f32_e32 v147, v147, v229
	v_exp_f32_e32 v144, v144
	v_exp_f32_e32 v145, v145
	v_exp_f32_e32 v146, v146
	v_exp_f32_e32 v147, v147
	v_add_f32_e32 v255, v144, v145
	v_add_f32_e32 v255, v255, v146
	v_add_f32_e32 v255, v255, v147
	s_waitcnt lgkmcnt(8)
	v_mfma_f32_32x32x16_bf16 v[0:15], v[168:171], v[204:207], v[0:15]
	v_cvt_pk_bf16_f32 v134, v140, v141
	v_cvt_pk_bf16_f32 v135, v142, v143
	v_sub_f32_e32 v148, v148, v229
	v_sub_f32_e32 v149, v149, v229
	v_sub_f32_e32 v150, v150, v229
	v_sub_f32_e32 v151, v151, v229
	v_exp_f32_e32 v148, v148
	v_exp_f32_e32 v149, v149
	v_exp_f32_e32 v150, v150
	s_waitcnt lgkmcnt(6)
	v_mfma_f32_32x32x16_bf16 v[64:79], v[172:175], v[176:179], v[64:79]
	v_exp_f32_e32 v151, v151
	v_add_f32_e32 v255, v255, v148
	v_add_f32_e32 v255, v255, v149
	v_add_f32_e32 v255, v255, v150
	v_add_f32_e32 v255, v255, v151
	v_cvt_pk_bf16_f32 v136, v144, v145
	v_cvt_pk_bf16_f32 v137, v146, v147
	v_sub_f32_e32 v152, v152, v229
	v_sub_f32_e32 v153, v153, v229
	s_waitcnt lgkmcnt(4)
	v_mfma_f32_32x32x16_bf16 v[32:47], v[172:175], v[180:183], v[32:47]
	v_sub_f32_e32 v154, v154, v229
	v_sub_f32_e32 v155, v155, v229
	v_exp_f32_e32 v152, v152
	v_exp_f32_e32 v153, v153
	v_exp_f32_e32 v154, v154
	v_exp_f32_e32 v155, v155
	v_add_f32_e32 v255, v255, v152
	v_add_f32_e32 v255, v255, v153
	s_waitcnt lgkmcnt(2)
	v_mfma_f32_32x32x16_bf16 v[16:31], v[172:175], v[184:187], v[16:31]
	v_add_f32_e32 v255, v255, v154
	v_add_f32_e32 v255, v255, v155
	v_cvt_pk_bf16_f32 v138, v148, v149
	v_cvt_pk_bf16_f32 v139, v150, v151
	v_sub_f32_e32 v156, v156, v229
	v_sub_f32_e32 v157, v157, v229
	v_sub_f32_e32 v158, v158, v229
	v_sub_f32_e32 v159, v159, v229
	v_exp_f32_e32 v156, v156
	s_waitcnt lgkmcnt(0)
	v_mfma_f32_32x32x16_bf16 v[0:15], v[172:175], v[188:191], v[0:15]
	v_exp_f32_e32 v157, v157
	v_exp_f32_e32 v158, v158
	v_exp_f32_e32 v159, v159
	v_add_f32_e32 v255, v255, v156
	v_add_f32_e32 v255, v255, v157
	v_add_f32_e32 v255, v255, v158
	v_add_f32_e32 v255, v255, v159
	v_cvt_pk_bf16_f32 v140, v152, v153
	v_cvt_pk_bf16_f32 v141, v154, v155
	v_cvt_pk_bf16_f32 v142, v156, v157
	v_cvt_pk_bf16_f32 v143, v158, v159
	v_add_f32_e32 v254, v254, v255
	v_mov_b32_e32 v255, v254
	s_nop 1
	v_permlane32_swap_b32_e32 v254, v255
	v_add_f32_e32 v254, v254, v255
	v_fma_f32 v208, v208, v228, v254
.Lattn_tail:
	s_addk_i32 s43, 0x4000
	s_add_i32 s41, s41, 1
	s_add_u32 s14, s14, 0x68000
	s_addc_u32 s15, s15, 0
	s_add_i32 s47, s47, 64
	v_add_u32_e32 v250, 0x100, v250
	s_cmp_lg_u32 s46, s14
	s_cbranch_scc1 .Lattn_loop
	s_add_i32 s17, s45, 1
	s_cmp_eq_u32 s17, s42
	s_cbranch_scc0 .Lattn_done
	ds_read_b64_tr_b16 v[192:193], v212 offset:32768
	ds_read_b64_tr_b16 v[194:195], v212 offset:34816
	ds_read_b64_tr_b16 v[196:197], v213 offset:32768
	ds_read_b64_tr_b16 v[198:199], v213 offset:34816
	ds_read_b64_tr_b16 v[200:201], v214 offset:32768
	ds_read_b64_tr_b16 v[202:203], v214 offset:34816
	ds_read_b64_tr_b16 v[204:205], v215 offset:32768
	ds_read_b64_tr_b16 v[206:207], v215 offset:34816
	ds_read_b64_tr_b16 v[144:145], v212 offset:36864
	ds_read_b64_tr_b16 v[146:147], v212 offset:38912
	ds_read_b64_tr_b16 v[148:149], v213 offset:36864
	ds_read_b64_tr_b16 v[150:151], v213 offset:38912
	ds_read_b64_tr_b16 v[152:153], v214 offset:36864
	ds_read_b64_tr_b16 v[154:155], v214 offset:38912
	s_waitcnt lgkmcnt(12)
	v_mfma_f32_32x32x16_bf16 v[112:127], v[128:131], v[192:195], v[112:127]
	ds_read_b64_tr_b16 v[156:157], v215 offset:36864
	ds_read_b64_tr_b16 v[158:159], v215 offset:38912
	s_waitcnt lgkmcnt(12)
	v_mfma_f32_32x32x16_bf16 v[96:111], v[128:131], v[196:199], v[96:111]
	ds_read_b64_tr_b16 v[160:161], v212 offset:40960
	ds_read_b64_tr_b16 v[162:163], v212 offset:43008
	s_waitcnt lgkmcnt(12)
	v_mfma_f32_32x32x16_bf16 v[80:95], v[128:131], v[200:203], v[80:95]
	ds_read_b64_tr_b16 v[164:165], v213 offset:40960
	ds_read_b64_tr_b16 v[166:167], v213 offset:43008
	s_waitcnt lgkmcnt(12)
	v_mfma_f32_32x32x16_bf16 v[48:63], v[128:131], v[204:207], v[48:63]
	ds_read_b64_tr_b16 v[168:169], v214 offset:40960
	ds_read_b64_tr_b16 v[170:171], v214 offset:43008
	s_waitcnt lgkmcnt(12)
	v_mfma_f32_32x32x16_bf16 v[112:127], v[132:135], v[144:147], v[112:127]
	ds_read_b64_tr_b16 v[172:173], v215 offset:40960
	ds_read_b64_tr_b16 v[174:175], v215 offset:43008
	s_waitcnt lgkmcnt(12)
	v_mfma_f32_32x32x16_bf16 v[96:111], v[132:135], v[148:151], v[96:111]
	ds_read_b64_tr_b16 v[176:177], v212 offset:45056
	ds_read_b64_tr_b16 v[178:179], v212 offset:47104
	s_waitcnt lgkmcnt(12)
	v_mfma_f32_32x32x16_bf16 v[80:95], v[132:135], v[152:155], v[80:95]
	ds_read_b64_tr_b16 v[180:181], v213 offset:45056
	ds_read_b64_tr_b16 v[182:183], v213 offset:47104
	s_waitcnt lgkmcnt(12)
	v_mfma_f32_32x32x16_bf16 v[48:63], v[132:135], v[156:159], v[48:63]
	ds_read_b64_tr_b16 v[184:185], v214 offset:45056
	ds_read_b64_tr_b16 v[186:187], v214 offset:47104
	s_waitcnt lgkmcnt(12)
	v_mfma_f32_32x32x16_bf16 v[112:127], v[136:139], v[160:163], v[112:127]
	ds_read_b64_tr_b16 v[188:189], v215 offset:45056
	ds_read_b64_tr_b16 v[190:191], v215 offset:47104
	s_waitcnt lgkmcnt(12)
	v_mfma_f32_32x32x16_bf16 v[96:111], v[136:139], v[164:167], v[96:111]
	s_waitcnt lgkmcnt(10)
	v_mfma_f32_32x32x16_bf16 v[80:95], v[136:139], v[168:171], v[80:95]
	s_waitcnt lgkmcnt(8)
	v_mfma_f32_32x32x16_bf16 v[48:63], v[136:139], v[172:175], v[48:63]
	s_waitcnt lgkmcnt(6)
	v_mfma_f32_32x32x16_bf16 v[112:127], v[140:143], v[176:179], v[112:127]
	s_waitcnt lgkmcnt(4)
	v_mfma_f32_32x32x16_bf16 v[96:111], v[140:143], v[180:183], v[96:111]
	s_waitcnt lgkmcnt(2)
	v_mfma_f32_32x32x16_bf16 v[80:95], v[140:143], v[184:187], v[80:95]
	s_waitcnt lgkmcnt(0)
	v_mfma_f32_32x32x16_bf16 v[48:63], v[140:143], v[188:191], v[48:63]
.Lattn_done:
	s_branch .LBB0_563
.LBB0_583:
	s_load_dwordx8 s[36:43], s[92:93], 0x110
	v_mov_b32_e32 v250, 0x3ecc95a3
	v_mov_b32_e32 v251, 0x7f800000
